# hand-written P6 top-k select row body: two-level find_bin, exec-mask passes, mbcnt compaction, counted vmcnt in final pass
# speedup vs baseline: 1.0232x; 1.0232x over previous
.LBB0_1234:
	s_or_b64 exec, exec, s[4:5]
	s_lshl_b64 s[4:5], s[38:39], 10
	s_add_u32 s40, s48, s4
	s_addc_u32 s41, s49, s5
	s_cmpk_gt_i32 s38, 0xff
	s_mov_b64 s[4:5], -1
	s_cbranch_scc0 .LBB0_1866
	s_add_i32 s2, s38, 1
	s_lshl_b64 s[42:43], s[38:39], 15
	s_add_u32 s42, s46, s42
	s_addc_u32 s43, s47, s43
	v_lshlrev_b32_e32 v58, 4, v50
	v_mov_b32_e32 v150, 0
	v_mov_b32_e32 v151, 0
	v_mov_b32_e32 v152, 0
	v_mov_b32_e32 v153, 0
	v_add_u32_e32 v64, s52, v58
	s_movk_i32 s15, 0x100
	s_mov_b64 s[8:9], s[42:43]
	global_load_dwordx4 v[2:5], v58, s[8:9]
	global_load_dwordx4 v[6:9], v58, s[8:9] offset:1024
	global_load_dwordx4 v[10:13], v58, s[8:9] offset:2048
	global_load_dwordx4 v[14:17], v58, s[8:9] offset:3072
	ds_write_b128 v64, v[150:153]
	ds_write_b128 v64, v[150:153] offset:1024
	ds_write_b128 v64, v[150:153] offset:2048
	ds_write_b128 v64, v[150:153] offset:3072
	ds_write_b128 v64, v[150:153] offset:4096
	ds_write_b128 v64, v[150:153] offset:5120
	ds_write_b128 v64, v[150:153] offset:6144
	ds_write_b128 v64, v[150:153] offset:7168
	s_mov_b32 s16, 0
	s_waitcnt vmcnt(0)
.Lsel_p1_loop:
	v_mov_b64_e32 v[18:19], v[2:3]
	v_mov_b64_e32 v[20:21], v[4:5]
	v_mov_b64_e32 v[22:23], v[6:7]
	v_mov_b64_e32 v[24:25], v[8:9]
	v_mov_b64_e32 v[26:27], v[10:11]
	v_mov_b64_e32 v[28:29], v[12:13]
	v_mov_b64_e32 v[30:31], v[14:15]
	v_mov_b64_e32 v[32:33], v[16:17]
	s_add_i32 s36, s16, 0x400
	s_cmp_lt_i32 s36, s2
	s_cbranch_scc0 .Lsel_p1_nold
	s_add_u32 s8, s8, 0x1000
	s_addc_u32 s9, s9, 0
	global_load_dwordx4 v[2:5], v58, s[8:9]
	global_load_dwordx4 v[6:9], v58, s[8:9] offset:1024
	global_load_dwordx4 v[10:13], v58, s[8:9] offset:2048
	global_load_dwordx4 v[14:17], v58, s[8:9] offset:3072
.Lsel_p1_nold:
	s_cmp_le_i32 s36, s2
	s_cbranch_scc0 .Lsel_p1_tail
	v_ashrrev_i32_e32 v34, 31, v18
	v_or_b32_e32 v34, 0x80000000, v34
	v_xor_b32_e32 v34, v18, v34
	v_bfe_u32 v34, v34, 21, 11
	v_lshl_add_u32 v34, v34, 2, s52
	ds_add_u32 v34, v57
	v_ashrrev_i32_e32 v35, 31, v19
	v_or_b32_e32 v35, 0x80000000, v35
	v_xor_b32_e32 v35, v19, v35
	v_bfe_u32 v35, v35, 21, 11
	v_lshl_add_u32 v35, v35, 2, s52
	ds_add_u32 v35, v57
	v_ashrrev_i32_e32 v36, 31, v20
	v_or_b32_e32 v36, 0x80000000, v36
	v_xor_b32_e32 v36, v20, v36
	v_bfe_u32 v36, v36, 21, 11
	v_lshl_add_u32 v36, v36, 2, s52
	ds_add_u32 v36, v57
	v_ashrrev_i32_e32 v37, 31, v21
	v_or_b32_e32 v37, 0x80000000, v37
	v_xor_b32_e32 v37, v21, v37
	v_bfe_u32 v37, v37, 21, 11
	v_lshl_add_u32 v37, v37, 2, s52
	ds_add_u32 v37, v57
	v_ashrrev_i32_e32 v38, 31, v22
	v_or_b32_e32 v38, 0x80000000, v38
	v_xor_b32_e32 v38, v22, v38
	v_bfe_u32 v38, v38, 21, 11
	v_lshl_add_u32 v38, v38, 2, s52
	ds_add_u32 v38, v57
	v_ashrrev_i32_e32 v39, 31, v23
	v_or_b32_e32 v39, 0x80000000, v39
	v_xor_b32_e32 v39, v23, v39
	v_bfe_u32 v39, v39, 21, 11
	v_lshl_add_u32 v39, v39, 2, s52
	ds_add_u32 v39, v57
	v_ashrrev_i32_e32 v40, 31, v24
	v_or_b32_e32 v40, 0x80000000, v40
	v_xor_b32_e32 v40, v24, v40
	v_bfe_u32 v40, v40, 21, 11
	v_lshl_add_u32 v40, v40, 2, s52
	ds_add_u32 v40, v57
	v_ashrrev_i32_e32 v41, 31, v25
	v_or_b32_e32 v41, 0x80000000, v41
	v_xor_b32_e32 v41, v25, v41
	v_bfe_u32 v41, v41, 21, 11
	v_lshl_add_u32 v41, v41, 2, s52
	ds_add_u32 v41, v57
	v_ashrrev_i32_e32 v42, 31, v26
	v_or_b32_e32 v42, 0x80000000, v42
	v_xor_b32_e32 v42, v26, v42
	v_bfe_u32 v42, v42, 21, 11
	v_lshl_add_u32 v42, v42, 2, s52
	ds_add_u32 v42, v57
	v_ashrrev_i32_e32 v43, 31, v27
	v_or_b32_e32 v43, 0x80000000, v43
	v_xor_b32_e32 v43, v27, v43
	v_bfe_u32 v43, v43, 21, 11
	v_lshl_add_u32 v43, v43, 2, s52
	ds_add_u32 v43, v57
	v_ashrrev_i32_e32 v44, 31, v28
	v_or_b32_e32 v44, 0x80000000, v44
	v_xor_b32_e32 v44, v28, v44
	v_bfe_u32 v44, v44, 21, 11
	v_lshl_add_u32 v44, v44, 2, s52
	ds_add_u32 v44, v57
	v_ashrrev_i32_e32 v45, 31, v29
	v_or_b32_e32 v45, 0x80000000, v45
	v_xor_b32_e32 v45, v29, v45
	v_bfe_u32 v45, v45, 21, 11
	v_lshl_add_u32 v45, v45, 2, s52
	ds_add_u32 v45, v57
	v_ashrrev_i32_e32 v46, 31, v30
	v_or_b32_e32 v46, 0x80000000, v46
	v_xor_b32_e32 v46, v30, v46
	v_bfe_u32 v46, v46, 21, 11
	v_lshl_add_u32 v46, v46, 2, s52
	ds_add_u32 v46, v57
	v_ashrrev_i32_e32 v47, 31, v31
	v_or_b32_e32 v47, 0x80000000, v47
	v_xor_b32_e32 v47, v31, v47
	v_bfe_u32 v47, v47, 21, 11
	v_lshl_add_u32 v47, v47, 2, s52
	ds_add_u32 v47, v57
	v_ashrrev_i32_e32 v48, 31, v32
	v_or_b32_e32 v48, 0x80000000, v48
	v_xor_b32_e32 v48, v32, v48
	v_bfe_u32 v48, v48, 21, 11
	v_lshl_add_u32 v48, v48, 2, s52
	ds_add_u32 v48, v57
	v_ashrrev_i32_e32 v49, 31, v33
	v_or_b32_e32 v49, 0x80000000, v49
	v_xor_b32_e32 v49, v33, v49
	v_bfe_u32 v49, v49, 21, 11
	v_lshl_add_u32 v49, v49, 2, s52
	ds_add_u32 v49, v57
	s_mov_b32 s16, s36
	s_cmp_lt_i32 s16, s2
	s_cbranch_scc0 .Lsel_p1_done
	s_waitcnt vmcnt(0)
	s_branch .Lsel_p1_loop
.Lsel_p1_tail:
	s_sub_i32 s37, s2, s16
	v_sub_u32_e32 v134, s37, v56
	v_cmpx_lt_i32_e32 vcc, 0, v134
	v_ashrrev_i32_e32 v34, 31, v18
	v_or_b32_e32 v34, 0x80000000, v34
	v_xor_b32_e32 v34, v18, v34
	v_bfe_u32 v34, v34, 21, 11
	v_lshl_add_u32 v34, v34, 2, s52
	ds_add_u32 v34, v57
	v_cmpx_lt_i32_e32 vcc, 1, v134
	v_ashrrev_i32_e32 v35, 31, v19
	v_or_b32_e32 v35, 0x80000000, v35
	v_xor_b32_e32 v35, v19, v35
	v_bfe_u32 v35, v35, 21, 11
	v_lshl_add_u32 v35, v35, 2, s52
	ds_add_u32 v35, v57
	v_cmpx_lt_i32_e32 vcc, 2, v134
	v_ashrrev_i32_e32 v36, 31, v20
	v_or_b32_e32 v36, 0x80000000, v36
	v_xor_b32_e32 v36, v20, v36
	v_bfe_u32 v36, v36, 21, 11
	v_lshl_add_u32 v36, v36, 2, s52
	ds_add_u32 v36, v57
	v_cmpx_lt_i32_e32 vcc, 3, v134
	v_ashrrev_i32_e32 v37, 31, v21
	v_or_b32_e32 v37, 0x80000000, v37
	v_xor_b32_e32 v37, v21, v37
	v_bfe_u32 v37, v37, 21, 11
	v_lshl_add_u32 v37, v37, 2, s52
	ds_add_u32 v37, v57
	v_cmpx_lt_i32_e32 vcc, 0x100, v134
	v_ashrrev_i32_e32 v38, 31, v22
	v_or_b32_e32 v38, 0x80000000, v38
	v_xor_b32_e32 v38, v22, v38
	v_bfe_u32 v38, v38, 21, 11
	v_lshl_add_u32 v38, v38, 2, s52
	ds_add_u32 v38, v57
	v_cmpx_lt_i32_e32 vcc, 0x101, v134
	v_ashrrev_i32_e32 v39, 31, v23
	v_or_b32_e32 v39, 0x80000000, v39
	v_xor_b32_e32 v39, v23, v39
	v_bfe_u32 v39, v39, 21, 11
	v_lshl_add_u32 v39, v39, 2, s52
	ds_add_u32 v39, v57
	v_cmpx_lt_i32_e32 vcc, 0x102, v134
	v_ashrrev_i32_e32 v40, 31, v24
	v_or_b32_e32 v40, 0x80000000, v40
	v_xor_b32_e32 v40, v24, v40
	v_bfe_u32 v40, v40, 21, 11
	v_lshl_add_u32 v40, v40, 2, s52
	ds_add_u32 v40, v57
	v_cmpx_lt_i32_e32 vcc, 0x103, v134
	v_ashrrev_i32_e32 v41, 31, v25
	v_or_b32_e32 v41, 0x80000000, v41
	v_xor_b32_e32 v41, v25, v41
	v_bfe_u32 v41, v41, 21, 11
	v_lshl_add_u32 v41, v41, 2, s52
	ds_add_u32 v41, v57
	v_cmpx_lt_i32_e32 vcc, 0x200, v134
	v_ashrrev_i32_e32 v42, 31, v26
	v_or_b32_e32 v42, 0x80000000, v42
	v_xor_b32_e32 v42, v26, v42
	v_bfe_u32 v42, v42, 21, 11
	v_lshl_add_u32 v42, v42, 2, s52
	ds_add_u32 v42, v57
	v_cmpx_lt_i32_e32 vcc, 0x201, v134
	v_ashrrev_i32_e32 v43, 31, v27
	v_or_b32_e32 v43, 0x80000000, v43
	v_xor_b32_e32 v43, v27, v43
	v_bfe_u32 v43, v43, 21, 11
	v_lshl_add_u32 v43, v43, 2, s52
	ds_add_u32 v43, v57
	v_cmpx_lt_i32_e32 vcc, 0x202, v134
	v_ashrrev_i32_e32 v44, 31, v28
	v_or_b32_e32 v44, 0x80000000, v44
	v_xor_b32_e32 v44, v28, v44
	v_bfe_u32 v44, v44, 21, 11
	v_lshl_add_u32 v44, v44, 2, s52
	ds_add_u32 v44, v57
	v_cmpx_lt_i32_e32 vcc, 0x203, v134
	v_ashrrev_i32_e32 v45, 31, v29
	v_or_b32_e32 v45, 0x80000000, v45
	v_xor_b32_e32 v45, v29, v45
	v_bfe_u32 v45, v45, 21, 11
	v_lshl_add_u32 v45, v45, 2, s52
	ds_add_u32 v45, v57
	v_cmpx_lt_i32_e32 vcc, 0x300, v134
	v_ashrrev_i32_e32 v46, 31, v30
	v_or_b32_e32 v46, 0x80000000, v46
	v_xor_b32_e32 v46, v30, v46
	v_bfe_u32 v46, v46, 21, 11
	v_lshl_add_u32 v46, v46, 2, s52
	ds_add_u32 v46, v57
	v_cmpx_lt_i32_e32 vcc, 0x301, v134
	v_ashrrev_i32_e32 v47, 31, v31
	v_or_b32_e32 v47, 0x80000000, v47
	v_xor_b32_e32 v47, v31, v47
	v_bfe_u32 v47, v47, 21, 11
	v_lshl_add_u32 v47, v47, 2, s52
	ds_add_u32 v47, v57
	v_cmpx_lt_i32_e32 vcc, 0x302, v134
	v_ashrrev_i32_e32 v48, 31, v32
	v_or_b32_e32 v48, 0x80000000, v48
	v_xor_b32_e32 v48, v32, v48
	v_bfe_u32 v48, v48, 21, 11
	v_lshl_add_u32 v48, v48, 2, s52
	ds_add_u32 v48, v57
	v_cmpx_lt_i32_e32 vcc, 0x303, v134
	v_ashrrev_i32_e32 v49, 31, v33
	v_or_b32_e32 v49, 0x80000000, v49
	v_xor_b32_e32 v49, v33, v49
	v_bfe_u32 v49, v49, 21, 11
	v_lshl_add_u32 v49, v49, 2, s52
	ds_add_u32 v49, v57
	s_mov_b64 exec, -1
.Lsel_p1_done:
	s_waitcnt lgkmcnt(0)
	v_lshl_add_u32 v34, v50, 7, s52
	ds_read_b128 v[2:5], v34
	ds_read_b128 v[6:9], v34 offset:16
	ds_read_b128 v[10:13], v34 offset:32
	ds_read_b128 v[14:17], v34 offset:48
	ds_read_b128 v[18:21], v34 offset:64
	ds_read_b128 v[22:25], v34 offset:80
	ds_read_b128 v[26:29], v34 offset:96
	ds_read_b128 v[30:33], v34 offset:112
	s_waitcnt lgkmcnt(0)
	v_add_u32_e32 v35, v2, v3
	v_add3_u32 v35, v35, v4, v5
	v_add3_u32 v35, v35, v6, v7
	v_add3_u32 v35, v35, v8, v9
	v_add3_u32 v35, v35, v10, v11
	v_add3_u32 v35, v35, v12, v13
	v_add3_u32 v35, v35, v14, v15
	v_add3_u32 v35, v35, v16, v17
	v_add3_u32 v35, v35, v18, v19
	v_add3_u32 v35, v35, v20, v21
	v_add3_u32 v35, v35, v22, v23
	v_add3_u32 v35, v35, v24, v25
	v_add3_u32 v35, v35, v26, v27
	v_add3_u32 v35, v35, v28, v29
	v_add3_u32 v35, v35, v30, v31
	v_add3_u32 v35, v35, v32, v33
	v_mov_b32_e32 v36, v35
	s_nop 1
	v_add_u32_dpp v36, v36, v36 row_shr:1 row_mask:0xf bank_mask:0xf bound_ctrl:1
	s_nop 1
	v_add_u32_dpp v36, v36, v36 row_shr:2 row_mask:0xf bank_mask:0xf bound_ctrl:1
	s_nop 1
	v_add_u32_dpp v36, v36, v36 row_shr:4 row_mask:0xf bank_mask:0xf bound_ctrl:1
	s_nop 1
	v_add_u32_dpp v36, v36, v36 row_shr:8 row_mask:0xf bank_mask:0xf bound_ctrl:1
	s_nop 1
	v_add_u32_dpp v36, v36, v36 row_bcast:15 row_mask:0xa bank_mask:0xf
	s_nop 1
	v_add_u32_dpp v36, v36, v36 row_bcast:31 row_mask:0xc bank_mask:0xf
	s_nop 0
	v_readlane_b32 s4, v36, 63
	s_nop 1
	v_sub_u32_e32 v37, s4, v36
	v_add_u32_e32 v38, v37, v35
	v_cmp_gt_u32_e32 vcc, s15, v37
	v_cmp_le_u32_e64 s[4:5], s15, v38
	s_and_b64 s[4:5], vcc, s[4:5]
	s_ff1_i32_b64 s6, s[4:5]
	v_readlane_b32 s7, v37, s6
	s_lshl_b32 s10, s6, 7
	s_add_i32 s10, s10, s52
	s_addk_i32 s10, 124
	v_and_b32_e32 v39, 31, v50
	v_lshlrev_b32_e32 v39, 2, v39
	v_sub_u32_e32 v39, s10, v39
	ds_read_b32 v40, v39
	v_cmp_gt_u32_e32 vcc, 32, v50
	s_waitcnt lgkmcnt(0)
	s_nop 1
	v_cndmask_b32_e32 v40, 0, v40, vcc
	v_mov_b32_e32 v41, v40
	s_nop 1
	v_add_u32_dpp v41, v41, v41 row_shr:1 row_mask:0xf bank_mask:0xf bound_ctrl:1
	s_nop 1
	v_add_u32_dpp v41, v41, v41 row_shr:2 row_mask:0xf bank_mask:0xf bound_ctrl:1
	s_nop 1
	v_add_u32_dpp v41, v41, v41 row_shr:4 row_mask:0xf bank_mask:0xf bound_ctrl:1
	s_nop 1
	v_add_u32_dpp v41, v41, v41 row_shr:8 row_mask:0xf bank_mask:0xf bound_ctrl:1
	s_nop 1
	v_add_u32_dpp v41, v41, v41 row_bcast:15 row_mask:0xa bank_mask:0xf
	s_nop 1
	v_add_u32_dpp v41, v41, v41 row_bcast:31 row_mask:0xc bank_mask:0xf
	s_nop 0
	v_sub_u32_e32 v42, v41, v40
	v_add_u32_e32 v42, s7, v42
	v_add_u32_e32 v43, v42, v40
	v_cmp_gt_u32_e32 vcc, s15, v42
	v_cmp_le_u32_e64 s[4:5], s15, v43
	s_and_b64 s[4:5], vcc, s[4:5]
	s_ff1_i32_b64 s11, s[4:5]
	v_readlane_b32 s14, v40, s11
	v_readlane_b32 s5, v42, s11
	s_lshl_b32 s13, s6, 5
	s_sub_i32 s4, 31, s11
	s_add_i32 s13, s13, s4
	s_sub_i32 s15, s15, s5
	s_mov_b64 s[8:9], s[42:43]
	global_load_dwordx4 v[2:5], v58, s[8:9]
	global_load_dwordx4 v[6:9], v58, s[8:9] offset:1024
	global_load_dwordx4 v[10:13], v58, s[8:9] offset:2048
	global_load_dwordx4 v[14:17], v58, s[8:9] offset:3072
	ds_write_b128 v64, v[150:153]
	ds_write_b128 v64, v[150:153] offset:1024
	ds_write_b128 v64, v[150:153] offset:2048
	ds_write_b128 v64, v[150:153] offset:3072
	ds_write_b128 v64, v[150:153] offset:4096
	ds_write_b128 v64, v[150:153] offset:5120
	ds_write_b128 v64, v[150:153] offset:6144
	ds_write_b128 v64, v[150:153] offset:7168
	s_cmpk_le_u32 s14, 0x800
	s_cselect_b32 s25, -1, 0
	s_add_i32 s24, s52, 0x2000
	s_mov_b32 s16, 0
	s_waitcnt vmcnt(0)

.Lsel_p2_nold:
	s_cmp_le_i32 s36, s2
	s_cbranch_scc0 .Lsel_p2_tail
	v_ashrrev_i32_e32 v34, 31, v18
	v_or_b32_e32 v34, 0x80000000, v34
	v_xor_b32_e32 v34, v18, v34
	v_lshrrev_b32_e32 v118, 21, v34
	v_ashrrev_i32_e32 v35, 31, v19
	v_or_b32_e32 v35, 0x80000000, v35
	v_xor_b32_e32 v35, v19, v35
	v_lshrrev_b32_e32 v119, 21, v35
	v_ashrrev_i32_e32 v36, 31, v20
	v_or_b32_e32 v36, 0x80000000, v36
	v_xor_b32_e32 v36, v20, v36
	v_lshrrev_b32_e32 v120, 21, v36
	v_ashrrev_i32_e32 v37, 31, v21
	v_or_b32_e32 v37, 0x80000000, v37
	v_xor_b32_e32 v37, v21, v37
	v_lshrrev_b32_e32 v121, 21, v37
	v_ashrrev_i32_e32 v38, 31, v22
	v_or_b32_e32 v38, 0x80000000, v38
	v_xor_b32_e32 v38, v22, v38
	v_lshrrev_b32_e32 v122, 21, v38
	v_ashrrev_i32_e32 v39, 31, v23
	v_or_b32_e32 v39, 0x80000000, v39
	v_xor_b32_e32 v39, v23, v39
	v_lshrrev_b32_e32 v123, 21, v39
	v_ashrrev_i32_e32 v40, 31, v24
	v_or_b32_e32 v40, 0x80000000, v40
	v_xor_b32_e32 v40, v24, v40
	v_lshrrev_b32_e32 v124, 21, v40
	v_ashrrev_i32_e32 v41, 31, v25
	v_or_b32_e32 v41, 0x80000000, v41
	v_xor_b32_e32 v41, v25, v41
	v_lshrrev_b32_e32 v125, 21, v41
	v_ashrrev_i32_e32 v42, 31, v26
	v_or_b32_e32 v42, 0x80000000, v42
	v_xor_b32_e32 v42, v26, v42
	v_lshrrev_b32_e32 v126, 21, v42
	v_ashrrev_i32_e32 v43, 31, v27
	v_or_b32_e32 v43, 0x80000000, v43
	v_xor_b32_e32 v43, v27, v43
	v_lshrrev_b32_e32 v127, 21, v43
	v_ashrrev_i32_e32 v44, 31, v28
	v_or_b32_e32 v44, 0x80000000, v44
	v_xor_b32_e32 v44, v28, v44
	v_lshrrev_b32_e32 v128, 21, v44
	v_ashrrev_i32_e32 v45, 31, v29
	v_or_b32_e32 v45, 0x80000000, v45
	v_xor_b32_e32 v45, v29, v45
	v_lshrrev_b32_e32 v129, 21, v45
	v_ashrrev_i32_e32 v46, 31, v30
	v_or_b32_e32 v46, 0x80000000, v46
	v_xor_b32_e32 v46, v30, v46
	v_lshrrev_b32_e32 v130, 21, v46
	v_ashrrev_i32_e32 v47, 31, v31
	v_or_b32_e32 v47, 0x80000000, v47
	v_xor_b32_e32 v47, v31, v47
	v_lshrrev_b32_e32 v131, 21, v47
	v_ashrrev_i32_e32 v48, 31, v32
	v_or_b32_e32 v48, 0x80000000, v48
	v_xor_b32_e32 v48, v32, v48
	v_lshrrev_b32_e32 v132, 21, v48
	v_ashrrev_i32_e32 v49, 31, v33
	v_or_b32_e32 v49, 0x80000000, v49
	v_xor_b32_e32 v49, v33, v49
	v_lshrrev_b32_e32 v133, 21, v49
	v_cmpx_eq_u32_e32 vcc, s13, v118
	v_bfe_u32 v118, v34, 10, 11
	v_lshl_add_u32 v118, v118, 2, s52
	ds_add_u32 v118, v57
	v_mbcnt_lo_u32_b32 v118, vcc_lo, 0
	v_mbcnt_hi_u32_b32 v118, vcc_hi, v118
	v_lshl_add_u32 v118, v118, 2, s24
	ds_write_b32 v118, v34
	s_bcnt1_i32_b64 s5, vcc
	s_and_b32 s5, s5, s25
	s_lshl2_add_u32 s24, s5, s24
	s_mov_b64 exec, -1
	v_cmpx_eq_u32_e32 vcc, s13, v119
	v_bfe_u32 v119, v35, 10, 11
	v_lshl_add_u32 v119, v119, 2, s52
	ds_add_u32 v119, v57
	v_mbcnt_lo_u32_b32 v119, vcc_lo, 0
	v_mbcnt_hi_u32_b32 v119, vcc_hi, v119
	v_lshl_add_u32 v119, v119, 2, s24
	ds_write_b32 v119, v35
	s_bcnt1_i32_b64 s5, vcc
	s_and_b32 s5, s5, s25
	s_lshl2_add_u32 s24, s5, s24
	s_mov_b64 exec, -1
	v_cmpx_eq_u32_e32 vcc, s13, v120
	v_bfe_u32 v120, v36, 10, 11
	v_lshl_add_u32 v120, v120, 2, s52
	ds_add_u32 v120, v57
	v_mbcnt_lo_u32_b32 v120, vcc_lo, 0
	v_mbcnt_hi_u32_b32 v120, vcc_hi, v120
	v_lshl_add_u32 v120, v120, 2, s24
	ds_write_b32 v120, v36
	s_bcnt1_i32_b64 s5, vcc
	s_and_b32 s5, s5, s25
	s_lshl2_add_u32 s24, s5, s24
	s_mov_b64 exec, -1
	v_cmpx_eq_u32_e32 vcc, s13, v121
	v_bfe_u32 v121, v37, 10, 11
	v_lshl_add_u32 v121, v121, 2, s52
	ds_add_u32 v121, v57
	v_mbcnt_lo_u32_b32 v121, vcc_lo, 0
	v_mbcnt_hi_u32_b32 v121, vcc_hi, v121
	v_lshl_add_u32 v121, v121, 2, s24
	ds_write_b32 v121, v37
	s_bcnt1_i32_b64 s5, vcc
	s_and_b32 s5, s5, s25
	s_lshl2_add_u32 s24, s5, s24
	s_mov_b64 exec, -1
	v_cmpx_eq_u32_e32 vcc, s13, v122
	v_bfe_u32 v122, v38, 10, 11
	v_lshl_add_u32 v122, v122, 2, s52
	ds_add_u32 v122, v57
	v_mbcnt_lo_u32_b32 v122, vcc_lo, 0
	v_mbcnt_hi_u32_b32 v122, vcc_hi, v122
	v_lshl_add_u32 v122, v122, 2, s24
	ds_write_b32 v122, v38
	s_bcnt1_i32_b64 s5, vcc
	s_and_b32 s5, s5, s25
	s_lshl2_add_u32 s24, s5, s24
	s_mov_b64 exec, -1
	v_cmpx_eq_u32_e32 vcc, s13, v123
	v_bfe_u32 v123, v39, 10, 11
	v_lshl_add_u32 v123, v123, 2, s52
	ds_add_u32 v123, v57
	v_mbcnt_lo_u32_b32 v123, vcc_lo, 0
	v_mbcnt_hi_u32_b32 v123, vcc_hi, v123
	v_lshl_add_u32 v123, v123, 2, s24
	ds_write_b32 v123, v39
	s_bcnt1_i32_b64 s5, vcc
	s_and_b32 s5, s5, s25
	s_lshl2_add_u32 s24, s5, s24
	s_mov_b64 exec, -1
	v_cmpx_eq_u32_e32 vcc, s13, v124
	v_bfe_u32 v124, v40, 10, 11
	v_lshl_add_u32 v124, v124, 2, s52
	ds_add_u32 v124, v57
	v_mbcnt_lo_u32_b32 v124, vcc_lo, 0
	v_mbcnt_hi_u32_b32 v124, vcc_hi, v124
	v_lshl_add_u32 v124, v124, 2, s24
	ds_write_b32 v124, v40
	s_bcnt1_i32_b64 s5, vcc
	s_and_b32 s5, s5, s25
	s_lshl2_add_u32 s24, s5, s24
	s_mov_b64 exec, -1
	v_cmpx_eq_u32_e32 vcc, s13, v125
	v_bfe_u32 v125, v41, 10, 11
	v_lshl_add_u32 v125, v125, 2, s52
	ds_add_u32 v125, v57
	v_mbcnt_lo_u32_b32 v125, vcc_lo, 0
	v_mbcnt_hi_u32_b32 v125, vcc_hi, v125
	v_lshl_add_u32 v125, v125, 2, s24
	ds_write_b32 v125, v41
	s_bcnt1_i32_b64 s5, vcc
	s_and_b32 s5, s5, s25
	s_lshl2_add_u32 s24, s5, s24
	s_mov_b64 exec, -1
	v_cmpx_eq_u32_e32 vcc, s13, v126
	v_bfe_u32 v126, v42, 10, 11
	v_lshl_add_u32 v126, v126, 2, s52
	ds_add_u32 v126, v57
	v_mbcnt_lo_u32_b32 v126, vcc_lo, 0
	v_mbcnt_hi_u32_b32 v126, vcc_hi, v126
	v_lshl_add_u32 v126, v126, 2, s24
	ds_write_b32 v126, v42
	s_bcnt1_i32_b64 s5, vcc
	s_and_b32 s5, s5, s25
	s_lshl2_add_u32 s24, s5, s24
	s_mov_b64 exec, -1
	v_cmpx_eq_u32_e32 vcc, s13, v127
	v_bfe_u32 v127, v43, 10, 11
	v_lshl_add_u32 v127, v127, 2, s52
	ds_add_u32 v127, v57
	v_mbcnt_lo_u32_b32 v127, vcc_lo, 0
	v_mbcnt_hi_u32_b32 v127, vcc_hi, v127
	v_lshl_add_u32 v127, v127, 2, s24
	ds_write_b32 v127, v43
	s_bcnt1_i32_b64 s5, vcc
	s_and_b32 s5, s5, s25
	s_lshl2_add_u32 s24, s5, s24
	s_mov_b64 exec, -1
	v_cmpx_eq_u32_e32 vcc, s13, v128
	v_bfe_u32 v128, v44, 10, 11
	v_lshl_add_u32 v128, v128, 2, s52
	ds_add_u32 v128, v57
	v_mbcnt_lo_u32_b32 v128, vcc_lo, 0
	v_mbcnt_hi_u32_b32 v128, vcc_hi, v128
	v_lshl_add_u32 v128, v128, 2, s24
	ds_write_b32 v128, v44
	s_bcnt1_i32_b64 s5, vcc
	s_and_b32 s5, s5, s25
	s_lshl2_add_u32 s24, s5, s24
	s_mov_b64 exec, -1
	v_cmpx_eq_u32_e32 vcc, s13, v129
	v_bfe_u32 v129, v45, 10, 11
	v_lshl_add_u32 v129, v129, 2, s52
	ds_add_u32 v129, v57
	v_mbcnt_lo_u32_b32 v129, vcc_lo, 0
	v_mbcnt_hi_u32_b32 v129, vcc_hi, v129
	v_lshl_add_u32 v129, v129, 2, s24
	ds_write_b32 v129, v45
	s_bcnt1_i32_b64 s5, vcc
	s_and_b32 s5, s5, s25
	s_lshl2_add_u32 s24, s5, s24
	s_mov_b64 exec, -1
	v_cmpx_eq_u32_e32 vcc, s13, v130
	v_bfe_u32 v130, v46, 10, 11
	v_lshl_add_u32 v130, v130, 2, s52
	ds_add_u32 v130, v57
	v_mbcnt_lo_u32_b32 v130, vcc_lo, 0
	v_mbcnt_hi_u32_b32 v130, vcc_hi, v130
	v_lshl_add_u32 v130, v130, 2, s24
	ds_write_b32 v130, v46
	s_bcnt1_i32_b64 s5, vcc
	s_and_b32 s5, s5, s25
	s_lshl2_add_u32 s24, s5, s24
	s_mov_b64 exec, -1
	v_cmpx_eq_u32_e32 vcc, s13, v131
	v_bfe_u32 v131, v47, 10, 11
	v_lshl_add_u32 v131, v131, 2, s52
	ds_add_u32 v131, v57
	v_mbcnt_lo_u32_b32 v131, vcc_lo, 0
	v_mbcnt_hi_u32_b32 v131, vcc_hi, v131
	v_lshl_add_u32 v131, v131, 2, s24
	ds_write_b32 v131, v47
	s_bcnt1_i32_b64 s5, vcc
	s_and_b32 s5, s5, s25
	s_lshl2_add_u32 s24, s5, s24
	s_mov_b64 exec, -1
	v_cmpx_eq_u32_e32 vcc, s13, v132
	v_bfe_u32 v132, v48, 10, 11
	v_lshl_add_u32 v132, v132, 2, s52
	ds_add_u32 v132, v57
	v_mbcnt_lo_u32_b32 v132, vcc_lo, 0
	v_mbcnt_hi_u32_b32 v132, vcc_hi, v132
	v_lshl_add_u32 v132, v132, 2, s24
	ds_write_b32 v132, v48
	s_bcnt1_i32_b64 s5, vcc
	s_and_b32 s5, s5, s25
	s_lshl2_add_u32 s24, s5, s24
	s_mov_b64 exec, -1
	v_cmpx_eq_u32_e32 vcc, s13, v133
	v_bfe_u32 v133, v49, 10, 11
	v_lshl_add_u32 v133, v133, 2, s52
	ds_add_u32 v133, v57
	v_mbcnt_lo_u32_b32 v133, vcc_lo, 0
	v_mbcnt_hi_u32_b32 v133, vcc_hi, v133
	v_lshl_add_u32 v133, v133, 2, s24
	ds_write_b32 v133, v49
	s_bcnt1_i32_b64 s5, vcc
	s_and_b32 s5, s5, s25
	s_lshl2_add_u32 s24, s5, s24
	s_mov_b64 exec, -1
	s_mov_b32 s16, s36
	s_cmp_lt_i32 s16, s2
	s_cbranch_scc0 .Lsel_p2_done
	s_waitcnt vmcnt(0)
	s_branch .Lsel_p2_loop
.Lsel_p2_tail:
	s_sub_i32 s37, s2, s16
	v_sub_u32_e32 v134, s37, v56
	v_ashrrev_i32_e32 v34, 31, v18
	v_or_b32_e32 v34, 0x80000000, v34
	v_xor_b32_e32 v34, v18, v34
	v_lshrrev_b32_e32 v118, 21, v34
	v_ashrrev_i32_e32 v35, 31, v19
	v_or_b32_e32 v35, 0x80000000, v35
	v_xor_b32_e32 v35, v19, v35
	v_lshrrev_b32_e32 v119, 21, v35
	v_ashrrev_i32_e32 v36, 31, v20
	v_or_b32_e32 v36, 0x80000000, v36
	v_xor_b32_e32 v36, v20, v36
	v_lshrrev_b32_e32 v120, 21, v36
	v_ashrrev_i32_e32 v37, 31, v21
	v_or_b32_e32 v37, 0x80000000, v37
	v_xor_b32_e32 v37, v21, v37
	v_lshrrev_b32_e32 v121, 21, v37
	v_ashrrev_i32_e32 v38, 31, v22
	v_or_b32_e32 v38, 0x80000000, v38
	v_xor_b32_e32 v38, v22, v38
	v_lshrrev_b32_e32 v122, 21, v38
	v_ashrrev_i32_e32 v39, 31, v23
	v_or_b32_e32 v39, 0x80000000, v39
	v_xor_b32_e32 v39, v23, v39
	v_lshrrev_b32_e32 v123, 21, v39
	v_ashrrev_i32_e32 v40, 31, v24
	v_or_b32_e32 v40, 0x80000000, v40
	v_xor_b32_e32 v40, v24, v40
	v_lshrrev_b32_e32 v124, 21, v40
	v_ashrrev_i32_e32 v41, 31, v25
	v_or_b32_e32 v41, 0x80000000, v41
	v_xor_b32_e32 v41, v25, v41
	v_lshrrev_b32_e32 v125, 21, v41
	v_ashrrev_i32_e32 v42, 31, v26
	v_or_b32_e32 v42, 0x80000000, v42
	v_xor_b32_e32 v42, v26, v42
	v_lshrrev_b32_e32 v126, 21, v42
	v_ashrrev_i32_e32 v43, 31, v27
	v_or_b32_e32 v43, 0x80000000, v43
	v_xor_b32_e32 v43, v27, v43
	v_lshrrev_b32_e32 v127, 21, v43
	v_ashrrev_i32_e32 v44, 31, v28
	v_or_b32_e32 v44, 0x80000000, v44
	v_xor_b32_e32 v44, v28, v44
	v_lshrrev_b32_e32 v128, 21, v44
	v_ashrrev_i32_e32 v45, 31, v29
	v_or_b32_e32 v45, 0x80000000, v45
	v_xor_b32_e32 v45, v29, v45
	v_lshrrev_b32_e32 v129, 21, v45
	v_ashrrev_i32_e32 v46, 31, v30
	v_or_b32_e32 v46, 0x80000000, v46
	v_xor_b32_e32 v46, v30, v46
	v_lshrrev_b32_e32 v130, 21, v46
	v_ashrrev_i32_e32 v47, 31, v31
	v_or_b32_e32 v47, 0x80000000, v47
	v_xor_b32_e32 v47, v31, v47
	v_lshrrev_b32_e32 v131, 21, v47
	v_ashrrev_i32_e32 v48, 31, v32
	v_or_b32_e32 v48, 0x80000000, v48
	v_xor_b32_e32 v48, v32, v48
	v_lshrrev_b32_e32 v132, 21, v48
	v_ashrrev_i32_e32 v49, 31, v33
	v_or_b32_e32 v49, 0x80000000, v49
	v_xor_b32_e32 v49, v33, v49
	v_lshrrev_b32_e32 v133, 21, v49
	v_cmpx_lt_i32_e32 vcc, 0, v134
	v_cmpx_eq_u32_e32 vcc, s13, v118
	v_bfe_u32 v118, v34, 10, 11
	v_lshl_add_u32 v118, v118, 2, s52
	ds_add_u32 v118, v57
	v_mbcnt_lo_u32_b32 v118, vcc_lo, 0
	v_mbcnt_hi_u32_b32 v118, vcc_hi, v118
	v_lshl_add_u32 v118, v118, 2, s24
	ds_write_b32 v118, v34
	s_bcnt1_i32_b64 s5, vcc
	s_and_b32 s5, s5, s25
	s_lshl2_add_u32 s24, s5, s24
	s_mov_b64 exec, -1
	v_cmpx_lt_i32_e32 vcc, 1, v134
	v_cmpx_eq_u32_e32 vcc, s13, v119
	v_bfe_u32 v119, v35, 10, 11
	v_lshl_add_u32 v119, v119, 2, s52
	ds_add_u32 v119, v57
	v_mbcnt_lo_u32_b32 v119, vcc_lo, 0
	v_mbcnt_hi_u32_b32 v119, vcc_hi, v119
	v_lshl_add_u32 v119, v119, 2, s24
	ds_write_b32 v119, v35
	s_bcnt1_i32_b64 s5, vcc
	s_and_b32 s5, s5, s25
	s_lshl2_add_u32 s24, s5, s24
	s_mov_b64 exec, -1
	v_cmpx_lt_i32_e32 vcc, 2, v134
	v_cmpx_eq_u32_e32 vcc, s13, v120
	v_bfe_u32 v120, v36, 10, 11
	v_lshl_add_u32 v120, v120, 2, s52
	ds_add_u32 v120, v57
	v_mbcnt_lo_u32_b32 v120, vcc_lo, 0
	v_mbcnt_hi_u32_b32 v120, vcc_hi, v120
	v_lshl_add_u32 v120, v120, 2, s24
	ds_write_b32 v120, v36
	s_bcnt1_i32_b64 s5, vcc
	s_and_b32 s5, s5, s25
	s_lshl2_add_u32 s24, s5, s24
	s_mov_b64 exec, -1
	v_cmpx_lt_i32_e32 vcc, 3, v134
	v_cmpx_eq_u32_e32 vcc, s13, v121
	v_bfe_u32 v121, v37, 10, 11
	v_lshl_add_u32 v121, v121, 2, s52
	ds_add_u32 v121, v57
	v_mbcnt_lo_u32_b32 v121, vcc_lo, 0
	v_mbcnt_hi_u32_b32 v121, vcc_hi, v121
	v_lshl_add_u32 v121, v121, 2, s24
	ds_write_b32 v121, v37
	s_bcnt1_i32_b64 s5, vcc
	s_and_b32 s5, s5, s25
	s_lshl2_add_u32 s24, s5, s24
	s_mov_b64 exec, -1
	v_cmpx_lt_i32_e32 vcc, 0x100, v134
	v_cmpx_eq_u32_e32 vcc, s13, v122
	v_bfe_u32 v122, v38, 10, 11
	v_lshl_add_u32 v122, v122, 2, s52
	ds_add_u32 v122, v57
	v_mbcnt_lo_u32_b32 v122, vcc_lo, 0
	v_mbcnt_hi_u32_b32 v122, vcc_hi, v122
	v_lshl_add_u32 v122, v122, 2, s24
	ds_write_b32 v122, v38
	s_bcnt1_i32_b64 s5, vcc
	s_and_b32 s5, s5, s25
	s_lshl2_add_u32 s24, s5, s24
	s_mov_b64 exec, -1
	v_cmpx_lt_i32_e32 vcc, 0x101, v134
	v_cmpx_eq_u32_e32 vcc, s13, v123
	v_bfe_u32 v123, v39, 10, 11
	v_lshl_add_u32 v123, v123, 2, s52
	ds_add_u32 v123, v57
	v_mbcnt_lo_u32_b32 v123, vcc_lo, 0
	v_mbcnt_hi_u32_b32 v123, vcc_hi, v123
	v_lshl_add_u32 v123, v123, 2, s24
	ds_write_b32 v123, v39
	s_bcnt1_i32_b64 s5, vcc
	s_and_b32 s5, s5, s25
	s_lshl2_add_u32 s24, s5, s24
	s_mov_b64 exec, -1
	v_cmpx_lt_i32_e32 vcc, 0x102, v134
	v_cmpx_eq_u32_e32 vcc, s13, v124
	v_bfe_u32 v124, v40, 10, 11
	v_lshl_add_u32 v124, v124, 2, s52
	ds_add_u32 v124, v57
	v_mbcnt_lo_u32_b32 v124, vcc_lo, 0
	v_mbcnt_hi_u32_b32 v124, vcc_hi, v124
	v_lshl_add_u32 v124, v124, 2, s24
	ds_write_b32 v124, v40
	s_bcnt1_i32_b64 s5, vcc
	s_and_b32 s5, s5, s25
	s_lshl2_add_u32 s24, s5, s24
	s_mov_b64 exec, -1
	v_cmpx_lt_i32_e32 vcc, 0x103, v134
	v_cmpx_eq_u32_e32 vcc, s13, v125
	v_bfe_u32 v125, v41, 10, 11
	v_lshl_add_u32 v125, v125, 2, s52
	ds_add_u32 v125, v57
	v_mbcnt_lo_u32_b32 v125, vcc_lo, 0
	v_mbcnt_hi_u32_b32 v125, vcc_hi, v125
	v_lshl_add_u32 v125, v125, 2, s24
	ds_write_b32 v125, v41
	s_bcnt1_i32_b64 s5, vcc
	s_and_b32 s5, s5, s25
	s_lshl2_add_u32 s24, s5, s24
	s_mov_b64 exec, -1
	v_cmpx_lt_i32_e32 vcc, 0x200, v134
	v_cmpx_eq_u32_e32 vcc, s13, v126
	v_bfe_u32 v126, v42, 10, 11
	v_lshl_add_u32 v126, v126, 2, s52
	ds_add_u32 v126, v57
	v_mbcnt_lo_u32_b32 v126, vcc_lo, 0
	v_mbcnt_hi_u32_b32 v126, vcc_hi, v126
	v_lshl_add_u32 v126, v126, 2, s24
	ds_write_b32 v126, v42
	s_bcnt1_i32_b64 s5, vcc
	s_and_b32 s5, s5, s25
	s_lshl2_add_u32 s24, s5, s24
	s_mov_b64 exec, -1
	v_cmpx_lt_i32_e32 vcc, 0x201, v134
	v_cmpx_eq_u32_e32 vcc, s13, v127
	v_bfe_u32 v127, v43, 10, 11
	v_lshl_add_u32 v127, v127, 2, s52
	ds_add_u32 v127, v57
	v_mbcnt_lo_u32_b32 v127, vcc_lo, 0
	v_mbcnt_hi_u32_b32 v127, vcc_hi, v127
	v_lshl_add_u32 v127, v127, 2, s24
	ds_write_b32 v127, v43
	s_bcnt1_i32_b64 s5, vcc
	s_and_b32 s5, s5, s25
	s_lshl2_add_u32 s24, s5, s24
	s_mov_b64 exec, -1
	v_cmpx_lt_i32_e32 vcc, 0x202, v134
	v_cmpx_eq_u32_e32 vcc, s13, v128
	v_bfe_u32 v128, v44, 10, 11
	v_lshl_add_u32 v128, v128, 2, s52
	ds_add_u32 v128, v57
	v_mbcnt_lo_u32_b32 v128, vcc_lo, 0
	v_mbcnt_hi_u32_b32 v128, vcc_hi, v128
	v_lshl_add_u32 v128, v128, 2, s24
	ds_write_b32 v128, v44
	s_bcnt1_i32_b64 s5, vcc
	s_and_b32 s5, s5, s25
	s_lshl2_add_u32 s24, s5, s24
	s_mov_b64 exec, -1
	v_cmpx_lt_i32_e32 vcc, 0x203, v134
	v_cmpx_eq_u32_e32 vcc, s13, v129
	v_bfe_u32 v129, v45, 10, 11
	v_lshl_add_u32 v129, v129, 2, s52
	ds_add_u32 v129, v57
	v_mbcnt_lo_u32_b32 v129, vcc_lo, 0
	v_mbcnt_hi_u32_b32 v129, vcc_hi, v129
	v_lshl_add_u32 v129, v129, 2, s24
	ds_write_b32 v129, v45
	s_bcnt1_i32_b64 s5, vcc
	s_and_b32 s5, s5, s25
	s_lshl2_add_u32 s24, s5, s24
	s_mov_b64 exec, -1
	v_cmpx_lt_i32_e32 vcc, 0x300, v134
	v_cmpx_eq_u32_e32 vcc, s13, v130
	v_bfe_u32 v130, v46, 10, 11
	v_lshl_add_u32 v130, v130, 2, s52
	ds_add_u32 v130, v57
	v_mbcnt_lo_u32_b32 v130, vcc_lo, 0
	v_mbcnt_hi_u32_b32 v130, vcc_hi, v130
	v_lshl_add_u32 v130, v130, 2, s24
	ds_write_b32 v130, v46
	s_bcnt1_i32_b64 s5, vcc
	s_and_b32 s5, s5, s25
	s_lshl2_add_u32 s24, s5, s24
	s_mov_b64 exec, -1
	v_cmpx_lt_i32_e32 vcc, 0x301, v134
	v_cmpx_eq_u32_e32 vcc, s13, v131
	v_bfe_u32 v131, v47, 10, 11
	v_lshl_add_u32 v131, v131, 2, s52
	ds_add_u32 v131, v57
	v_mbcnt_lo_u32_b32 v131, vcc_lo, 0
	v_mbcnt_hi_u32_b32 v131, vcc_hi, v131
	v_lshl_add_u32 v131, v131, 2, s24
	ds_write_b32 v131, v47
	s_bcnt1_i32_b64 s5, vcc
	s_and_b32 s5, s5, s25
	s_lshl2_add_u32 s24, s5, s24
	s_mov_b64 exec, -1
	v_cmpx_lt_i32_e32 vcc, 0x302, v134
	v_cmpx_eq_u32_e32 vcc, s13, v132
	v_bfe_u32 v132, v48, 10, 11
	v_lshl_add_u32 v132, v132, 2, s52
	ds_add_u32 v132, v57
	v_mbcnt_lo_u32_b32 v132, vcc_lo, 0
	v_mbcnt_hi_u32_b32 v132, vcc_hi, v132
	v_lshl_add_u32 v132, v132, 2, s24
	ds_write_b32 v132, v48
	s_bcnt1_i32_b64 s5, vcc
	s_and_b32 s5, s5, s25
	s_lshl2_add_u32 s24, s5, s24
	s_mov_b64 exec, -1
	v_cmpx_lt_i32_e32 vcc, 0x303, v134
	v_cmpx_eq_u32_e32 vcc, s13, v133
	v_bfe_u32 v133, v49, 10, 11
	v_lshl_add_u32 v133, v133, 2, s52
	ds_add_u32 v133, v57
	v_mbcnt_lo_u32_b32 v133, vcc_lo, 0
	v_mbcnt_hi_u32_b32 v133, vcc_hi, v133
	v_lshl_add_u32 v133, v133, 2, s24
	ds_write_b32 v133, v49
	s_bcnt1_i32_b64 s5, vcc
	s_and_b32 s5, s5, s25
	s_lshl2_add_u32 s24, s5, s24
	s_mov_b64 exec, -1
.Lsel_p2_done:
	s_waitcnt lgkmcnt(0)
	v_lshl_add_u32 v34, v50, 7, s52
	ds_read_b128 v[2:5], v34
	ds_read_b128 v[6:9], v34 offset:16
	ds_read_b128 v[10:13], v34 offset:32
	ds_read_b128 v[14:17], v34 offset:48
	ds_read_b128 v[18:21], v34 offset:64
	ds_read_b128 v[22:25], v34 offset:80
	ds_read_b128 v[26:29], v34 offset:96
	ds_read_b128 v[30:33], v34 offset:112
	s_waitcnt lgkmcnt(0)
	v_add_u32_e32 v35, v2, v3
	v_add3_u32 v35, v35, v4, v5
	v_add3_u32 v35, v35, v6, v7
	v_add3_u32 v35, v35, v8, v9
	v_add3_u32 v35, v35, v10, v11
	v_add3_u32 v35, v35, v12, v13
	v_add3_u32 v35, v35, v14, v15
	v_add3_u32 v35, v35, v16, v17
	v_add3_u32 v35, v35, v18, v19
	v_add3_u32 v35, v35, v20, v21
	v_add3_u32 v35, v35, v22, v23
	v_add3_u32 v35, v35, v24, v25
	v_add3_u32 v35, v35, v26, v27
	v_add3_u32 v35, v35, v28, v29
	v_add3_u32 v35, v35, v30, v31
	v_add3_u32 v35, v35, v32, v33
	v_mov_b32_e32 v36, v35
	s_nop 1
	v_add_u32_dpp v36, v36, v36 row_shr:1 row_mask:0xf bank_mask:0xf bound_ctrl:1
	s_nop 1
	v_add_u32_dpp v36, v36, v36 row_shr:2 row_mask:0xf bank_mask:0xf bound_ctrl:1
	s_nop 1
	v_add_u32_dpp v36, v36, v36 row_shr:4 row_mask:0xf bank_mask:0xf bound_ctrl:1
	s_nop 1
	v_add_u32_dpp v36, v36, v36 row_shr:8 row_mask:0xf bank_mask:0xf bound_ctrl:1
	s_nop 1
	v_add_u32_dpp v36, v36, v36 row_bcast:15 row_mask:0xa bank_mask:0xf
	s_nop 1
	v_add_u32_dpp v36, v36, v36 row_bcast:31 row_mask:0xc bank_mask:0xf
	s_nop 0
	v_readlane_b32 s4, v36, 63
	s_nop 1
	v_sub_u32_e32 v37, s4, v36
	v_add_u32_e32 v38, v37, v35
	v_cmp_gt_u32_e32 vcc, s15, v37
	v_cmp_le_u32_e64 s[4:5], s15, v38
	s_and_b64 s[4:5], vcc, s[4:5]
	s_ff1_i32_b64 s6, s[4:5]
	v_readlane_b32 s7, v37, s6
	s_lshl_b32 s10, s6, 7
	s_add_i32 s10, s10, s52
	s_addk_i32 s10, 124
	v_and_b32_e32 v39, 31, v50
	v_lshlrev_b32_e32 v39, 2, v39
	v_sub_u32_e32 v39, s10, v39
	ds_read_b32 v40, v39
	v_cmp_gt_u32_e32 vcc, 32, v50
	s_waitcnt lgkmcnt(0)
	s_nop 1
	v_cndmask_b32_e32 v40, 0, v40, vcc
	v_mov_b32_e32 v41, v40
	s_nop 1
	v_add_u32_dpp v41, v41, v41 row_shr:1 row_mask:0xf bank_mask:0xf bound_ctrl:1
	s_nop 1
	v_add_u32_dpp v41, v41, v41 row_shr:2 row_mask:0xf bank_mask:0xf bound_ctrl:1
	s_nop 1
	v_add_u32_dpp v41, v41, v41 row_shr:4 row_mask:0xf bank_mask:0xf bound_ctrl:1
	s_nop 1
	v_add_u32_dpp v41, v41, v41 row_shr:8 row_mask:0xf bank_mask:0xf bound_ctrl:1
	s_nop 1
	v_add_u32_dpp v41, v41, v41 row_bcast:15 row_mask:0xa bank_mask:0xf
	s_nop 1
	v_add_u32_dpp v41, v41, v41 row_bcast:31 row_mask:0xc bank_mask:0xf
	s_nop 0
	v_sub_u32_e32 v42, v41, v40
	v_add_u32_e32 v42, s7, v42
	v_add_u32_e32 v43, v42, v40
	v_cmp_gt_u32_e32 vcc, s15, v42
	v_cmp_le_u32_e64 s[4:5], s15, v43
	s_and_b64 s[4:5], vcc, s[4:5]
	s_ff1_i32_b64 s11, s[4:5]
	v_readlane_b32 s29, v40, s11
	v_readlane_b32 s5, v42, s11
	s_lshl_b32 s28, s6, 5
	s_sub_i32 s4, 31, s11
	s_add_i32 s28, s28, s4
	s_sub_i32 s15, s15, s5
	s_lshl_b32 s4, s13, 11
	s_or_b32 s17, s4, s28
	ds_write_b128 v64, v[150:153]
	ds_write_b128 v64, v[150:153] offset:1024
	ds_write_b128 v64, v[150:153] offset:2048
	ds_write_b128 v64, v[150:153] offset:3072
	s_cmp_lg_u32 s25, 0
	s_cbranch_scc0 .Lsel_p3_row
	s_mov_b32 s10, 0
.Lsel_p3_loop:
	v_add_u32_e32 v34, s10, v50
	v_cmpx_gt_u32_e32 vcc, s14, v34
	v_lshl_add_u32 v35, v34, 2, s52
	ds_read_b32 v36, v35 offset:8192
	s_waitcnt lgkmcnt(0)
	v_lshrrev_b32_e32 v37, 10, v36
	v_cmpx_eq_u32_e32 vcc, s17, v37
	v_and_b32_e32 v37, 0x3ff, v36
	v_lshl_add_u32 v37, v37, 2, s52
	ds_add_u32 v37, v57
	s_mov_b64 exec, -1
	s_add_i32 s10, s10, 64
	s_cmp_lt_u32 s10, s14
	s_cbranch_scc1 .Lsel_p3_loop
	s_branch .Lsel_p3_done
.Lsel_p3_row:
	s_mov_b32 s10, 0
.Lsel_p3_rloop:
	v_add_u32_e32 v34, s10, v50
	v_cmpx_gt_i32_e32 vcc, s2, v34
	v_lshlrev_b32_e32 v35, 2, v34
	global_load_dword v36, v35, s[42:43]
	s_waitcnt vmcnt(0)
	v_ashrrev_i32_e32 v38, 31, v36
	v_or_b32_e32 v38, 0x80000000, v38
	v_xor_b32_e32 v38, v36, v38
	v_lshrrev_b32_e32 v37, 10, v38
	v_cmpx_eq_u32_e32 vcc, s17, v37
	v_and_b32_e32 v37, 0x3ff, v38
	v_lshl_add_u32 v37, v37, 2, s52
	ds_add_u32 v37, v57
	s_mov_b64 exec, -1
	s_add_i32 s10, s10, 64
	s_cmp_lt_i32 s10, s2
	s_cbranch_scc1 .Lsel_p3_rloop
.Lsel_p3_done:
	s_waitcnt lgkmcnt(0)
	v_lshl_add_u32 v34, v50, 6, s52
	ds_read_b128 v[2:5], v34
	ds_read_b128 v[6:9], v34 offset:16
	ds_read_b128 v[10:13], v34 offset:32
	ds_read_b128 v[14:17], v34 offset:48
	s_waitcnt lgkmcnt(0)
	v_add_u32_e32 v35, v2, v3
	v_add3_u32 v35, v35, v4, v5
	v_add3_u32 v35, v35, v6, v7
	v_add3_u32 v35, v35, v8, v9
	v_add3_u32 v35, v35, v10, v11
	v_add3_u32 v35, v35, v12, v13
	v_add3_u32 v35, v35, v14, v15
	v_add3_u32 v35, v35, v16, v17
	v_mov_b32_e32 v36, v35
	s_nop 1
	v_add_u32_dpp v36, v36, v36 row_shr:1 row_mask:0xf bank_mask:0xf bound_ctrl:1
	s_nop 1
	v_add_u32_dpp v36, v36, v36 row_shr:2 row_mask:0xf bank_mask:0xf bound_ctrl:1
	s_nop 1
	v_add_u32_dpp v36, v36, v36 row_shr:4 row_mask:0xf bank_mask:0xf bound_ctrl:1
	s_nop 1
	v_add_u32_dpp v36, v36, v36 row_shr:8 row_mask:0xf bank_mask:0xf bound_ctrl:1
	s_nop 1
	v_add_u32_dpp v36, v36, v36 row_bcast:15 row_mask:0xa bank_mask:0xf
	s_nop 1
	v_add_u32_dpp v36, v36, v36 row_bcast:31 row_mask:0xc bank_mask:0xf
	s_nop 0
	v_readlane_b32 s4, v36, 63
	s_nop 1
	v_sub_u32_e32 v37, s4, v36
	v_add_u32_e32 v38, v37, v35
	v_cmp_gt_u32_e32 vcc, s15, v37
	v_cmp_le_u32_e64 s[4:5], s15, v38
	s_and_b64 s[4:5], vcc, s[4:5]
	s_ff1_i32_b64 s6, s[4:5]
	v_readlane_b32 s7, v37, s6
	s_lshl_b32 s10, s6, 6
	s_add_i32 s10, s10, s52
	s_addk_i32 s10, 60
	v_and_b32_e32 v39, 15, v50
	v_lshlrev_b32_e32 v39, 2, v39
	v_sub_u32_e32 v39, s10, v39
	ds_read_b32 v40, v39
	v_cmp_gt_u32_e32 vcc, 16, v50
	s_waitcnt lgkmcnt(0)
	s_nop 1
	v_cndmask_b32_e32 v40, 0, v40, vcc
	v_mov_b32_e32 v41, v40
	s_nop 1
	v_add_u32_dpp v41, v41, v41 row_shr:1 row_mask:0xf bank_mask:0xf bound_ctrl:1
	s_nop 1
	v_add_u32_dpp v41, v41, v41 row_shr:2 row_mask:0xf bank_mask:0xf bound_ctrl:1
	s_nop 1
	v_add_u32_dpp v41, v41, v41 row_shr:4 row_mask:0xf bank_mask:0xf bound_ctrl:1
	s_nop 1
	v_add_u32_dpp v41, v41, v41 row_shr:8 row_mask:0xf bank_mask:0xf bound_ctrl:1
	s_nop 1
	v_add_u32_dpp v41, v41, v41 row_bcast:15 row_mask:0xa bank_mask:0xf
	s_nop 1
	v_add_u32_dpp v41, v41, v41 row_bcast:31 row_mask:0xc bank_mask:0xf
	s_nop 0
	v_sub_u32_e32 v42, v41, v40
	v_add_u32_e32 v42, s7, v42
	v_add_u32_e32 v43, v42, v40
	v_cmp_gt_u32_e32 vcc, s15, v42
	v_cmp_le_u32_e64 s[4:5], s15, v43
	s_and_b64 s[4:5], vcc, s[4:5]
	s_ff1_i32_b64 s11, s[4:5]
	v_readlane_b32 s29, v40, s11
	v_readlane_b32 s5, v42, s11
	s_lshl_b32 s28, s6, 4
	s_sub_i32 s4, 15, s11
	s_add_i32 s28, s28, s4
	s_sub_i32 s15, s15, s5
	s_lshl_b32 s17, s17, 10
	s_or_b32 s17, s17, s28
	s_mov_b32 s26, 0
	s_mov_b32 s27, 0
	s_mov_b64 s[8:9], s[42:43]
	global_load_dwordx4 v[2:5], v58, s[8:9]
	global_load_dwordx4 v[6:9], v58, s[8:9] offset:1024
	global_load_dwordx4 v[10:13], v58, s[8:9] offset:2048
	global_load_dwordx4 v[14:17], v58, s[8:9] offset:3072
	s_mov_b32 s16, 0
	s_waitcnt vmcnt(0)

.Lsel_fin_nold:
	s_cmp_le_i32 s36, s2
	s_cbranch_scc0 .Lsel_fin_tail
	v_add_u32_e32 v145, s16, v56
	v_ashrrev_i32_e32 v34, 31, v18
	v_or_b32_e32 v34, 0x80000000, v34
	v_xor_b32_e32 v34, v18, v34
	v_ashrrev_i32_e32 v35, 31, v19
	v_or_b32_e32 v35, 0x80000000, v35
	v_xor_b32_e32 v35, v19, v35
	v_ashrrev_i32_e32 v36, 31, v20
	v_or_b32_e32 v36, 0x80000000, v36
	v_xor_b32_e32 v36, v20, v36
	v_ashrrev_i32_e32 v37, 31, v21
	v_or_b32_e32 v37, 0x80000000, v37
	v_xor_b32_e32 v37, v21, v37
	v_cmp_lt_u32_e64 s[58:59], s17, v34
	v_cmp_eq_u32_e64 s[66:67], s17, v34
	v_cmp_lt_u32_e64 s[60:61], s17, v35
	v_cmp_eq_u32_e64 s[68:69], s17, v35
	v_cmp_lt_u32_e64 s[62:63], s17, v36
	v_cmp_eq_u32_e64 s[72:73], s17, v36
	v_cmp_lt_u32_e64 s[64:65], s17, v37
	v_cmp_eq_u32_e64 s[74:75], s17, v37
	s_or_b64 s[4:5], s[66:67], s[68:69]
	s_or_b64 s[6:7], s[72:73], s[74:75]
	s_or_b64 s[4:5], s[4:5], s[6:7]
	s_cmp_lg_u64 s[4:5], 0
	s_cbranch_scc0 .Lsel_ff_st0
	v_mov_b32_e32 v136, s27
	v_mbcnt_lo_u32_b32 v136, s66, v136
	v_mbcnt_hi_u32_b32 v136, s67, v136
	v_mbcnt_lo_u32_b32 v136, s68, v136
	v_mbcnt_hi_u32_b32 v136, s69, v136
	v_mbcnt_lo_u32_b32 v136, s72, v136
	v_mbcnt_hi_u32_b32 v136, s73, v136
	v_mbcnt_lo_u32_b32 v136, s74, v136
	v_mbcnt_hi_u32_b32 v136, s75, v136
	s_mov_b64 exec, s[66:67]
	v_cmp_gt_u32_e64 s[4:5], s15, v136
	v_add_u32_e32 v136, 1, v136
	s_or_b64 s[58:59], s[58:59], s[4:5]
	s_mov_b64 exec, s[68:69]
	v_cmp_gt_u32_e64 s[4:5], s15, v136
	v_add_u32_e32 v136, 1, v136
	s_or_b64 s[60:61], s[60:61], s[4:5]
	s_mov_b64 exec, s[72:73]
	v_cmp_gt_u32_e64 s[4:5], s15, v136
	v_add_u32_e32 v136, 1, v136
	s_or_b64 s[62:63], s[62:63], s[4:5]
	s_mov_b64 exec, s[74:75]
	v_cmp_gt_u32_e64 s[4:5], s15, v136
	v_add_u32_e32 v136, 1, v136
	s_or_b64 s[64:65], s[64:65], s[4:5]
	s_mov_b64 exec, -1
	s_bcnt1_i32_b64 s4, s[66:67]
	s_add_i32 s27, s27, s4
	s_bcnt1_i32_b64 s4, s[68:69]
	s_add_i32 s27, s27, s4
	s_bcnt1_i32_b64 s4, s[72:73]
	s_add_i32 s27, s27, s4
	s_bcnt1_i32_b64 s4, s[74:75]
	s_add_i32 s27, s27, s4
.Lsel_ff_st0:
	v_mov_b32_e32 v135, s26
	v_mbcnt_lo_u32_b32 v135, s58, v135
	v_mbcnt_hi_u32_b32 v135, s59, v135
	v_mbcnt_lo_u32_b32 v135, s60, v135
	v_mbcnt_hi_u32_b32 v135, s61, v135
	v_mbcnt_lo_u32_b32 v135, s62, v135
	v_mbcnt_hi_u32_b32 v135, s63, v135
	v_mbcnt_lo_u32_b32 v135, s64, v135
	v_mbcnt_hi_u32_b32 v135, s65, v135
	s_mov_b64 exec, s[58:59]
	v_lshlrev_b32_e32 v137, 2, v135
	v_add_u32_e32 v135, 1, v135
	v_add_u32_e32 v141, 0, v145
	v_cmpx_gt_u32_e32 vcc, 0x400, v137
	global_store_dword v137, v141, s[40:41]
	s_mov_b64 exec, s[60:61]
	v_lshlrev_b32_e32 v138, 2, v135
	v_add_u32_e32 v135, 1, v135
	v_add_u32_e32 v142, 1, v145
	v_cmpx_gt_u32_e32 vcc, 0x400, v138
	global_store_dword v138, v142, s[40:41]
	s_mov_b64 exec, s[62:63]
	v_lshlrev_b32_e32 v139, 2, v135
	v_add_u32_e32 v135, 1, v135
	v_add_u32_e32 v143, 2, v145
	v_cmpx_gt_u32_e32 vcc, 0x400, v139
	global_store_dword v139, v143, s[40:41]
	s_mov_b64 exec, s[64:65]
	v_lshlrev_b32_e32 v140, 2, v135
	v_add_u32_e32 v135, 1, v135
	v_add_u32_e32 v144, 3, v145
	v_cmpx_gt_u32_e32 vcc, 0x400, v140
	global_store_dword v140, v144, s[40:41]
	s_mov_b64 exec, -1
	s_bcnt1_i32_b64 s4, s[58:59]
	s_add_i32 s26, s26, s4
	s_bcnt1_i32_b64 s4, s[60:61]
	s_add_i32 s26, s26, s4
	s_bcnt1_i32_b64 s4, s[62:63]
	s_add_i32 s26, s26, s4
	s_bcnt1_i32_b64 s4, s[64:65]
	s_add_i32 s26, s26, s4
	v_ashrrev_i32_e32 v38, 31, v22
	v_or_b32_e32 v38, 0x80000000, v38
	v_xor_b32_e32 v38, v22, v38
	v_ashrrev_i32_e32 v39, 31, v23
	v_or_b32_e32 v39, 0x80000000, v39
	v_xor_b32_e32 v39, v23, v39
	v_ashrrev_i32_e32 v40, 31, v24
	v_or_b32_e32 v40, 0x80000000, v40
	v_xor_b32_e32 v40, v24, v40
	v_ashrrev_i32_e32 v41, 31, v25
	v_or_b32_e32 v41, 0x80000000, v41
	v_xor_b32_e32 v41, v25, v41
	v_cmp_lt_u32_e64 s[58:59], s17, v38
	v_cmp_eq_u32_e64 s[66:67], s17, v38
	v_cmp_lt_u32_e64 s[60:61], s17, v39
	v_cmp_eq_u32_e64 s[68:69], s17, v39
	v_cmp_lt_u32_e64 s[62:63], s17, v40
	v_cmp_eq_u32_e64 s[72:73], s17, v40
	v_cmp_lt_u32_e64 s[64:65], s17, v41
	v_cmp_eq_u32_e64 s[74:75], s17, v41
	s_or_b64 s[4:5], s[66:67], s[68:69]
	s_or_b64 s[6:7], s[72:73], s[74:75]
	s_or_b64 s[4:5], s[4:5], s[6:7]
	s_cmp_lg_u64 s[4:5], 0
	s_cbranch_scc0 .Lsel_ff_st1
	v_mov_b32_e32 v136, s27
	v_mbcnt_lo_u32_b32 v136, s66, v136
	v_mbcnt_hi_u32_b32 v136, s67, v136
	v_mbcnt_lo_u32_b32 v136, s68, v136
	v_mbcnt_hi_u32_b32 v136, s69, v136
	v_mbcnt_lo_u32_b32 v136, s72, v136
	v_mbcnt_hi_u32_b32 v136, s73, v136
	v_mbcnt_lo_u32_b32 v136, s74, v136
	v_mbcnt_hi_u32_b32 v136, s75, v136
	s_mov_b64 exec, s[66:67]
	v_cmp_gt_u32_e64 s[4:5], s15, v136
	v_add_u32_e32 v136, 1, v136
	s_or_b64 s[58:59], s[58:59], s[4:5]
	s_mov_b64 exec, s[68:69]
	v_cmp_gt_u32_e64 s[4:5], s15, v136
	v_add_u32_e32 v136, 1, v136
	s_or_b64 s[60:61], s[60:61], s[4:5]
	s_mov_b64 exec, s[72:73]
	v_cmp_gt_u32_e64 s[4:5], s15, v136
	v_add_u32_e32 v136, 1, v136
	s_or_b64 s[62:63], s[62:63], s[4:5]
	s_mov_b64 exec, s[74:75]
	v_cmp_gt_u32_e64 s[4:5], s15, v136
	v_add_u32_e32 v136, 1, v136
	s_or_b64 s[64:65], s[64:65], s[4:5]
	s_mov_b64 exec, -1
	s_bcnt1_i32_b64 s4, s[66:67]
	s_add_i32 s27, s27, s4
	s_bcnt1_i32_b64 s4, s[68:69]
	s_add_i32 s27, s27, s4
	s_bcnt1_i32_b64 s4, s[72:73]
	s_add_i32 s27, s27, s4
	s_bcnt1_i32_b64 s4, s[74:75]
	s_add_i32 s27, s27, s4
.Lsel_ff_st1:
	v_mov_b32_e32 v135, s26
	v_mbcnt_lo_u32_b32 v135, s58, v135
	v_mbcnt_hi_u32_b32 v135, s59, v135
	v_mbcnt_lo_u32_b32 v135, s60, v135
	v_mbcnt_hi_u32_b32 v135, s61, v135
	v_mbcnt_lo_u32_b32 v135, s62, v135
	v_mbcnt_hi_u32_b32 v135, s63, v135
	v_mbcnt_lo_u32_b32 v135, s64, v135
	v_mbcnt_hi_u32_b32 v135, s65, v135
	s_mov_b64 exec, s[58:59]
	v_lshlrev_b32_e32 v137, 2, v135
	v_add_u32_e32 v135, 1, v135
	v_add_u32_e32 v141, 0x100, v145
	v_cmpx_gt_u32_e32 vcc, 0x400, v137
	global_store_dword v137, v141, s[40:41]
	s_mov_b64 exec, s[60:61]
	v_lshlrev_b32_e32 v138, 2, v135
	v_add_u32_e32 v135, 1, v135
	v_add_u32_e32 v142, 0x101, v145
	v_cmpx_gt_u32_e32 vcc, 0x400, v138
	global_store_dword v138, v142, s[40:41]
	s_mov_b64 exec, s[62:63]
	v_lshlrev_b32_e32 v139, 2, v135
	v_add_u32_e32 v135, 1, v135
	v_add_u32_e32 v143, 0x102, v145
	v_cmpx_gt_u32_e32 vcc, 0x400, v139
	global_store_dword v139, v143, s[40:41]
	s_mov_b64 exec, s[64:65]
	v_lshlrev_b32_e32 v140, 2, v135
	v_add_u32_e32 v135, 1, v135
	v_add_u32_e32 v144, 0x103, v145
	v_cmpx_gt_u32_e32 vcc, 0x400, v140
	global_store_dword v140, v144, s[40:41]
	s_mov_b64 exec, -1
	s_bcnt1_i32_b64 s4, s[58:59]
	s_add_i32 s26, s26, s4
	s_bcnt1_i32_b64 s4, s[60:61]
	s_add_i32 s26, s26, s4
	s_bcnt1_i32_b64 s4, s[62:63]
	s_add_i32 s26, s26, s4
	s_bcnt1_i32_b64 s4, s[64:65]
	s_add_i32 s26, s26, s4
	v_ashrrev_i32_e32 v42, 31, v26
	v_or_b32_e32 v42, 0x80000000, v42
	v_xor_b32_e32 v42, v26, v42
	v_ashrrev_i32_e32 v43, 31, v27
	v_or_b32_e32 v43, 0x80000000, v43
	v_xor_b32_e32 v43, v27, v43
	v_ashrrev_i32_e32 v44, 31, v28
	v_or_b32_e32 v44, 0x80000000, v44
	v_xor_b32_e32 v44, v28, v44
	v_ashrrev_i32_e32 v45, 31, v29
	v_or_b32_e32 v45, 0x80000000, v45
	v_xor_b32_e32 v45, v29, v45
	v_cmp_lt_u32_e64 s[58:59], s17, v42
	v_cmp_eq_u32_e64 s[66:67], s17, v42
	v_cmp_lt_u32_e64 s[60:61], s17, v43
	v_cmp_eq_u32_e64 s[68:69], s17, v43
	v_cmp_lt_u32_e64 s[62:63], s17, v44
	v_cmp_eq_u32_e64 s[72:73], s17, v44
	v_cmp_lt_u32_e64 s[64:65], s17, v45
	v_cmp_eq_u32_e64 s[74:75], s17, v45
	s_or_b64 s[4:5], s[66:67], s[68:69]
	s_or_b64 s[6:7], s[72:73], s[74:75]
	s_or_b64 s[4:5], s[4:5], s[6:7]
	s_cmp_lg_u64 s[4:5], 0
	s_cbranch_scc0 .Lsel_ff_st2
	v_mov_b32_e32 v136, s27
	v_mbcnt_lo_u32_b32 v136, s66, v136
	v_mbcnt_hi_u32_b32 v136, s67, v136
	v_mbcnt_lo_u32_b32 v136, s68, v136
	v_mbcnt_hi_u32_b32 v136, s69, v136
	v_mbcnt_lo_u32_b32 v136, s72, v136
	v_mbcnt_hi_u32_b32 v136, s73, v136
	v_mbcnt_lo_u32_b32 v136, s74, v136
	v_mbcnt_hi_u32_b32 v136, s75, v136
	s_mov_b64 exec, s[66:67]
	v_cmp_gt_u32_e64 s[4:5], s15, v136
	v_add_u32_e32 v136, 1, v136
	s_or_b64 s[58:59], s[58:59], s[4:5]
	s_mov_b64 exec, s[68:69]
	v_cmp_gt_u32_e64 s[4:5], s15, v136
	v_add_u32_e32 v136, 1, v136
	s_or_b64 s[60:61], s[60:61], s[4:5]
	s_mov_b64 exec, s[72:73]
	v_cmp_gt_u32_e64 s[4:5], s15, v136
	v_add_u32_e32 v136, 1, v136
	s_or_b64 s[62:63], s[62:63], s[4:5]
	s_mov_b64 exec, s[74:75]
	v_cmp_gt_u32_e64 s[4:5], s15, v136
	v_add_u32_e32 v136, 1, v136
	s_or_b64 s[64:65], s[64:65], s[4:5]
	s_mov_b64 exec, -1
	s_bcnt1_i32_b64 s4, s[66:67]
	s_add_i32 s27, s27, s4
	s_bcnt1_i32_b64 s4, s[68:69]
	s_add_i32 s27, s27, s4
	s_bcnt1_i32_b64 s4, s[72:73]
	s_add_i32 s27, s27, s4
	s_bcnt1_i32_b64 s4, s[74:75]
	s_add_i32 s27, s27, s4
.Lsel_ff_st2:
	v_mov_b32_e32 v135, s26
	v_mbcnt_lo_u32_b32 v135, s58, v135
	v_mbcnt_hi_u32_b32 v135, s59, v135
	v_mbcnt_lo_u32_b32 v135, s60, v135
	v_mbcnt_hi_u32_b32 v135, s61, v135
	v_mbcnt_lo_u32_b32 v135, s62, v135
	v_mbcnt_hi_u32_b32 v135, s63, v135
	v_mbcnt_lo_u32_b32 v135, s64, v135
	v_mbcnt_hi_u32_b32 v135, s65, v135
	s_mov_b64 exec, s[58:59]
	v_lshlrev_b32_e32 v137, 2, v135
	v_add_u32_e32 v135, 1, v135
	v_add_u32_e32 v141, 0x200, v145
	v_cmpx_gt_u32_e32 vcc, 0x400, v137
	global_store_dword v137, v141, s[40:41]
	s_mov_b64 exec, s[60:61]
	v_lshlrev_b32_e32 v138, 2, v135
	v_add_u32_e32 v135, 1, v135
	v_add_u32_e32 v142, 0x201, v145
	v_cmpx_gt_u32_e32 vcc, 0x400, v138
	global_store_dword v138, v142, s[40:41]
	s_mov_b64 exec, s[62:63]
	v_lshlrev_b32_e32 v139, 2, v135
	v_add_u32_e32 v135, 1, v135
	v_add_u32_e32 v143, 0x202, v145
	v_cmpx_gt_u32_e32 vcc, 0x400, v139
	global_store_dword v139, v143, s[40:41]
	s_mov_b64 exec, s[64:65]
	v_lshlrev_b32_e32 v140, 2, v135
	v_add_u32_e32 v135, 1, v135
	v_add_u32_e32 v144, 0x203, v145
	v_cmpx_gt_u32_e32 vcc, 0x400, v140
	global_store_dword v140, v144, s[40:41]
	s_mov_b64 exec, -1
	s_bcnt1_i32_b64 s4, s[58:59]
	s_add_i32 s26, s26, s4
	s_bcnt1_i32_b64 s4, s[60:61]
	s_add_i32 s26, s26, s4
	s_bcnt1_i32_b64 s4, s[62:63]
	s_add_i32 s26, s26, s4
	s_bcnt1_i32_b64 s4, s[64:65]
	s_add_i32 s26, s26, s4
	v_ashrrev_i32_e32 v46, 31, v30
	v_or_b32_e32 v46, 0x80000000, v46
	v_xor_b32_e32 v46, v30, v46
	v_ashrrev_i32_e32 v47, 31, v31
	v_or_b32_e32 v47, 0x80000000, v47
	v_xor_b32_e32 v47, v31, v47
	v_ashrrev_i32_e32 v48, 31, v32
	v_or_b32_e32 v48, 0x80000000, v48
	v_xor_b32_e32 v48, v32, v48
	v_ashrrev_i32_e32 v49, 31, v33
	v_or_b32_e32 v49, 0x80000000, v49
	v_xor_b32_e32 v49, v33, v49
	v_cmp_lt_u32_e64 s[58:59], s17, v46
	v_cmp_eq_u32_e64 s[66:67], s17, v46
	v_cmp_lt_u32_e64 s[60:61], s17, v47
	v_cmp_eq_u32_e64 s[68:69], s17, v47
	v_cmp_lt_u32_e64 s[62:63], s17, v48
	v_cmp_eq_u32_e64 s[72:73], s17, v48
	v_cmp_lt_u32_e64 s[64:65], s17, v49
	v_cmp_eq_u32_e64 s[74:75], s17, v49
	s_or_b64 s[4:5], s[66:67], s[68:69]
	s_or_b64 s[6:7], s[72:73], s[74:75]
	s_or_b64 s[4:5], s[4:5], s[6:7]
	s_cmp_lg_u64 s[4:5], 0
	s_cbranch_scc0 .Lsel_ff_st3
	v_mov_b32_e32 v136, s27
	v_mbcnt_lo_u32_b32 v136, s66, v136
	v_mbcnt_hi_u32_b32 v136, s67, v136
	v_mbcnt_lo_u32_b32 v136, s68, v136
	v_mbcnt_hi_u32_b32 v136, s69, v136
	v_mbcnt_lo_u32_b32 v136, s72, v136
	v_mbcnt_hi_u32_b32 v136, s73, v136
	v_mbcnt_lo_u32_b32 v136, s74, v136
	v_mbcnt_hi_u32_b32 v136, s75, v136
	s_mov_b64 exec, s[66:67]
	v_cmp_gt_u32_e64 s[4:5], s15, v136
	v_add_u32_e32 v136, 1, v136
	s_or_b64 s[58:59], s[58:59], s[4:5]
	s_mov_b64 exec, s[68:69]
	v_cmp_gt_u32_e64 s[4:5], s15, v136
	v_add_u32_e32 v136, 1, v136
	s_or_b64 s[60:61], s[60:61], s[4:5]
	s_mov_b64 exec, s[72:73]
	v_cmp_gt_u32_e64 s[4:5], s15, v136
	v_add_u32_e32 v136, 1, v136
	s_or_b64 s[62:63], s[62:63], s[4:5]
	s_mov_b64 exec, s[74:75]
	v_cmp_gt_u32_e64 s[4:5], s15, v136
	v_add_u32_e32 v136, 1, v136
	s_or_b64 s[64:65], s[64:65], s[4:5]
	s_mov_b64 exec, -1
	s_bcnt1_i32_b64 s4, s[66:67]
	s_add_i32 s27, s27, s4
	s_bcnt1_i32_b64 s4, s[68:69]
	s_add_i32 s27, s27, s4
	s_bcnt1_i32_b64 s4, s[72:73]
	s_add_i32 s27, s27, s4
	s_bcnt1_i32_b64 s4, s[74:75]
	s_add_i32 s27, s27, s4
.Lsel_ff_st3:
	v_mov_b32_e32 v135, s26
	v_mbcnt_lo_u32_b32 v135, s58, v135
	v_mbcnt_hi_u32_b32 v135, s59, v135
	v_mbcnt_lo_u32_b32 v135, s60, v135
	v_mbcnt_hi_u32_b32 v135, s61, v135
	v_mbcnt_lo_u32_b32 v135, s62, v135
	v_mbcnt_hi_u32_b32 v135, s63, v135
	v_mbcnt_lo_u32_b32 v135, s64, v135
	v_mbcnt_hi_u32_b32 v135, s65, v135
	s_mov_b64 exec, s[58:59]
	v_lshlrev_b32_e32 v137, 2, v135
	v_add_u32_e32 v135, 1, v135
	v_add_u32_e32 v141, 0x300, v145
	v_cmpx_gt_u32_e32 vcc, 0x400, v137
	global_store_dword v137, v141, s[40:41]
	s_mov_b64 exec, s[60:61]
	v_lshlrev_b32_e32 v138, 2, v135
	v_add_u32_e32 v135, 1, v135
	v_add_u32_e32 v142, 0x301, v145
	v_cmpx_gt_u32_e32 vcc, 0x400, v138
	global_store_dword v138, v142, s[40:41]
	s_mov_b64 exec, s[62:63]
	v_lshlrev_b32_e32 v139, 2, v135
	v_add_u32_e32 v135, 1, v135
	v_add_u32_e32 v143, 0x302, v145
	v_cmpx_gt_u32_e32 vcc, 0x400, v139
	global_store_dword v139, v143, s[40:41]
	s_mov_b64 exec, s[64:65]
	v_lshlrev_b32_e32 v140, 2, v135
	v_add_u32_e32 v135, 1, v135
	v_add_u32_e32 v144, 0x303, v145
	v_cmpx_gt_u32_e32 vcc, 0x400, v140
	global_store_dword v140, v144, s[40:41]
	s_mov_b64 exec, -1
	s_bcnt1_i32_b64 s4, s[58:59]
	s_add_i32 s26, s26, s4
	s_bcnt1_i32_b64 s4, s[60:61]
	s_add_i32 s26, s26, s4
	s_bcnt1_i32_b64 s4, s[62:63]
	s_add_i32 s26, s26, s4
	s_bcnt1_i32_b64 s4, s[64:65]
	s_add_i32 s26, s26, s4
	s_mov_b32 s16, s36
	s_cmp_lt_i32 s16, s2
	s_cbranch_scc0 .Lsel_fin_done
	s_waitcnt vmcnt(16)
	s_branch .Lsel_fin_loop
.Lsel_fin_tail:
	s_sub_i32 s37, s2, s16
	v_sub_u32_e32 v134, s37, v56
	v_add_u32_e32 v145, s16, v56
	v_ashrrev_i32_e32 v34, 31, v18
	v_or_b32_e32 v34, 0x80000000, v34
	v_xor_b32_e32 v34, v18, v34
	v_ashrrev_i32_e32 v35, 31, v19
	v_or_b32_e32 v35, 0x80000000, v35
	v_xor_b32_e32 v35, v19, v35
	v_ashrrev_i32_e32 v36, 31, v20
	v_or_b32_e32 v36, 0x80000000, v36
	v_xor_b32_e32 v36, v20, v36
	v_ashrrev_i32_e32 v37, 31, v21
	v_or_b32_e32 v37, 0x80000000, v37
	v_xor_b32_e32 v37, v21, v37
	v_cmpx_lt_i32_e32 vcc, 0, v134
	v_cmp_lt_u32_e64 s[58:59], s17, v34
	v_cmp_eq_u32_e64 s[66:67], s17, v34
	v_cmpx_lt_i32_e32 vcc, 1, v134
	v_cmp_lt_u32_e64 s[60:61], s17, v35
	v_cmp_eq_u32_e64 s[68:69], s17, v35
	v_cmpx_lt_i32_e32 vcc, 2, v134
	v_cmp_lt_u32_e64 s[62:63], s17, v36
	v_cmp_eq_u32_e64 s[72:73], s17, v36
	v_cmpx_lt_i32_e32 vcc, 3, v134
	v_cmp_lt_u32_e64 s[64:65], s17, v37
	v_cmp_eq_u32_e64 s[74:75], s17, v37
	s_mov_b64 exec, -1
	s_or_b64 s[4:5], s[66:67], s[68:69]
	s_or_b64 s[6:7], s[72:73], s[74:75]
	s_or_b64 s[4:5], s[4:5], s[6:7]
	s_cmp_lg_u64 s[4:5], 0
	s_cbranch_scc0 .Lsel_ft_st0
	v_mov_b32_e32 v136, s27
	v_mbcnt_lo_u32_b32 v136, s66, v136
	v_mbcnt_hi_u32_b32 v136, s67, v136
	v_mbcnt_lo_u32_b32 v136, s68, v136
	v_mbcnt_hi_u32_b32 v136, s69, v136
	v_mbcnt_lo_u32_b32 v136, s72, v136
	v_mbcnt_hi_u32_b32 v136, s73, v136
	v_mbcnt_lo_u32_b32 v136, s74, v136
	v_mbcnt_hi_u32_b32 v136, s75, v136
	s_mov_b64 exec, s[66:67]
	v_cmp_gt_u32_e64 s[4:5], s15, v136
	v_add_u32_e32 v136, 1, v136
	s_or_b64 s[58:59], s[58:59], s[4:5]
	s_mov_b64 exec, s[68:69]
	v_cmp_gt_u32_e64 s[4:5], s15, v136
	v_add_u32_e32 v136, 1, v136
	s_or_b64 s[60:61], s[60:61], s[4:5]
	s_mov_b64 exec, s[72:73]
	v_cmp_gt_u32_e64 s[4:5], s15, v136
	v_add_u32_e32 v136, 1, v136
	s_or_b64 s[62:63], s[62:63], s[4:5]
	s_mov_b64 exec, s[74:75]
	v_cmp_gt_u32_e64 s[4:5], s15, v136
	v_add_u32_e32 v136, 1, v136
	s_or_b64 s[64:65], s[64:65], s[4:5]
	s_mov_b64 exec, -1
	s_bcnt1_i32_b64 s4, s[66:67]
	s_add_i32 s27, s27, s4
	s_bcnt1_i32_b64 s4, s[68:69]
	s_add_i32 s27, s27, s4
	s_bcnt1_i32_b64 s4, s[72:73]
	s_add_i32 s27, s27, s4
	s_bcnt1_i32_b64 s4, s[74:75]
	s_add_i32 s27, s27, s4
.Lsel_ft_st0:
	v_mov_b32_e32 v135, s26
	v_mbcnt_lo_u32_b32 v135, s58, v135
	v_mbcnt_hi_u32_b32 v135, s59, v135
	v_mbcnt_lo_u32_b32 v135, s60, v135
	v_mbcnt_hi_u32_b32 v135, s61, v135
	v_mbcnt_lo_u32_b32 v135, s62, v135
	v_mbcnt_hi_u32_b32 v135, s63, v135
	v_mbcnt_lo_u32_b32 v135, s64, v135
	v_mbcnt_hi_u32_b32 v135, s65, v135
	s_mov_b64 exec, s[58:59]
	v_lshlrev_b32_e32 v137, 2, v135
	v_add_u32_e32 v135, 1, v135
	v_add_u32_e32 v141, 0, v145
	v_cmpx_gt_u32_e32 vcc, 0x400, v137
	global_store_dword v137, v141, s[40:41]
	s_mov_b64 exec, s[60:61]
	v_lshlrev_b32_e32 v138, 2, v135
	v_add_u32_e32 v135, 1, v135
	v_add_u32_e32 v142, 1, v145
	v_cmpx_gt_u32_e32 vcc, 0x400, v138
	global_store_dword v138, v142, s[40:41]
	s_mov_b64 exec, s[62:63]
	v_lshlrev_b32_e32 v139, 2, v135
	v_add_u32_e32 v135, 1, v135
	v_add_u32_e32 v143, 2, v145
	v_cmpx_gt_u32_e32 vcc, 0x400, v139
	global_store_dword v139, v143, s[40:41]
	s_mov_b64 exec, s[64:65]
	v_lshlrev_b32_e32 v140, 2, v135
	v_add_u32_e32 v135, 1, v135
	v_add_u32_e32 v144, 3, v145
	v_cmpx_gt_u32_e32 vcc, 0x400, v140
	global_store_dword v140, v144, s[40:41]
	s_mov_b64 exec, -1
	s_bcnt1_i32_b64 s4, s[58:59]
	s_add_i32 s26, s26, s4
	s_bcnt1_i32_b64 s4, s[60:61]
	s_add_i32 s26, s26, s4
	s_bcnt1_i32_b64 s4, s[62:63]
	s_add_i32 s26, s26, s4
	s_bcnt1_i32_b64 s4, s[64:65]
	s_add_i32 s26, s26, s4
	v_ashrrev_i32_e32 v38, 31, v22
	v_or_b32_e32 v38, 0x80000000, v38
	v_xor_b32_e32 v38, v22, v38
	v_ashrrev_i32_e32 v39, 31, v23
	v_or_b32_e32 v39, 0x80000000, v39
	v_xor_b32_e32 v39, v23, v39
	v_ashrrev_i32_e32 v40, 31, v24
	v_or_b32_e32 v40, 0x80000000, v40
	v_xor_b32_e32 v40, v24, v40
	v_ashrrev_i32_e32 v41, 31, v25
	v_or_b32_e32 v41, 0x80000000, v41
	v_xor_b32_e32 v41, v25, v41
	v_cmpx_lt_i32_e32 vcc, 0x100, v134
	v_cmp_lt_u32_e64 s[58:59], s17, v38
	v_cmp_eq_u32_e64 s[66:67], s17, v38
	v_cmpx_lt_i32_e32 vcc, 0x101, v134
	v_cmp_lt_u32_e64 s[60:61], s17, v39
	v_cmp_eq_u32_e64 s[68:69], s17, v39
	v_cmpx_lt_i32_e32 vcc, 0x102, v134
	v_cmp_lt_u32_e64 s[62:63], s17, v40
	v_cmp_eq_u32_e64 s[72:73], s17, v40
	v_cmpx_lt_i32_e32 vcc, 0x103, v134
	v_cmp_lt_u32_e64 s[64:65], s17, v41
	v_cmp_eq_u32_e64 s[74:75], s17, v41
	s_mov_b64 exec, -1
	s_or_b64 s[4:5], s[66:67], s[68:69]
	s_or_b64 s[6:7], s[72:73], s[74:75]
	s_or_b64 s[4:5], s[4:5], s[6:7]
	s_cmp_lg_u64 s[4:5], 0
	s_cbranch_scc0 .Lsel_ft_st1
	v_mov_b32_e32 v136, s27
	v_mbcnt_lo_u32_b32 v136, s66, v136
	v_mbcnt_hi_u32_b32 v136, s67, v136
	v_mbcnt_lo_u32_b32 v136, s68, v136
	v_mbcnt_hi_u32_b32 v136, s69, v136
	v_mbcnt_lo_u32_b32 v136, s72, v136
	v_mbcnt_hi_u32_b32 v136, s73, v136
	v_mbcnt_lo_u32_b32 v136, s74, v136
	v_mbcnt_hi_u32_b32 v136, s75, v136
	s_mov_b64 exec, s[66:67]
	v_cmp_gt_u32_e64 s[4:5], s15, v136
	v_add_u32_e32 v136, 1, v136
	s_or_b64 s[58:59], s[58:59], s[4:5]
	s_mov_b64 exec, s[68:69]
	v_cmp_gt_u32_e64 s[4:5], s15, v136
	v_add_u32_e32 v136, 1, v136
	s_or_b64 s[60:61], s[60:61], s[4:5]
	s_mov_b64 exec, s[72:73]
	v_cmp_gt_u32_e64 s[4:5], s15, v136
	v_add_u32_e32 v136, 1, v136
	s_or_b64 s[62:63], s[62:63], s[4:5]
	s_mov_b64 exec, s[74:75]
	v_cmp_gt_u32_e64 s[4:5], s15, v136
	v_add_u32_e32 v136, 1, v136
	s_or_b64 s[64:65], s[64:65], s[4:5]
	s_mov_b64 exec, -1
	s_bcnt1_i32_b64 s4, s[66:67]
	s_add_i32 s27, s27, s4
	s_bcnt1_i32_b64 s4, s[68:69]
	s_add_i32 s27, s27, s4
	s_bcnt1_i32_b64 s4, s[72:73]
	s_add_i32 s27, s27, s4
	s_bcnt1_i32_b64 s4, s[74:75]
	s_add_i32 s27, s27, s4
.Lsel_ft_st1:
	v_mov_b32_e32 v135, s26
	v_mbcnt_lo_u32_b32 v135, s58, v135
	v_mbcnt_hi_u32_b32 v135, s59, v135
	v_mbcnt_lo_u32_b32 v135, s60, v135
	v_mbcnt_hi_u32_b32 v135, s61, v135
	v_mbcnt_lo_u32_b32 v135, s62, v135
	v_mbcnt_hi_u32_b32 v135, s63, v135
	v_mbcnt_lo_u32_b32 v135, s64, v135
	v_mbcnt_hi_u32_b32 v135, s65, v135
	s_mov_b64 exec, s[58:59]
	v_lshlrev_b32_e32 v137, 2, v135
	v_add_u32_e32 v135, 1, v135
	v_add_u32_e32 v141, 0x100, v145
	v_cmpx_gt_u32_e32 vcc, 0x400, v137
	global_store_dword v137, v141, s[40:41]
	s_mov_b64 exec, s[60:61]
	v_lshlrev_b32_e32 v138, 2, v135
	v_add_u32_e32 v135, 1, v135
	v_add_u32_e32 v142, 0x101, v145
	v_cmpx_gt_u32_e32 vcc, 0x400, v138
	global_store_dword v138, v142, s[40:41]
	s_mov_b64 exec, s[62:63]
	v_lshlrev_b32_e32 v139, 2, v135
	v_add_u32_e32 v135, 1, v135
	v_add_u32_e32 v143, 0x102, v145
	v_cmpx_gt_u32_e32 vcc, 0x400, v139
	global_store_dword v139, v143, s[40:41]
	s_mov_b64 exec, s[64:65]
	v_lshlrev_b32_e32 v140, 2, v135
	v_add_u32_e32 v135, 1, v135
	v_add_u32_e32 v144, 0x103, v145
	v_cmpx_gt_u32_e32 vcc, 0x400, v140
	global_store_dword v140, v144, s[40:41]
	s_mov_b64 exec, -1
	s_bcnt1_i32_b64 s4, s[58:59]
	s_add_i32 s26, s26, s4
	s_bcnt1_i32_b64 s4, s[60:61]
	s_add_i32 s26, s26, s4
	s_bcnt1_i32_b64 s4, s[62:63]
	s_add_i32 s26, s26, s4
	s_bcnt1_i32_b64 s4, s[64:65]
	s_add_i32 s26, s26, s4
	v_ashrrev_i32_e32 v42, 31, v26
	v_or_b32_e32 v42, 0x80000000, v42
	v_xor_b32_e32 v42, v26, v42
	v_ashrrev_i32_e32 v43, 31, v27
	v_or_b32_e32 v43, 0x80000000, v43
	v_xor_b32_e32 v43, v27, v43
	v_ashrrev_i32_e32 v44, 31, v28
	v_or_b32_e32 v44, 0x80000000, v44
	v_xor_b32_e32 v44, v28, v44
	v_ashrrev_i32_e32 v45, 31, v29
	v_or_b32_e32 v45, 0x80000000, v45
	v_xor_b32_e32 v45, v29, v45
	v_cmpx_lt_i32_e32 vcc, 0x200, v134
	v_cmp_lt_u32_e64 s[58:59], s17, v42
	v_cmp_eq_u32_e64 s[66:67], s17, v42
	v_cmpx_lt_i32_e32 vcc, 0x201, v134
	v_cmp_lt_u32_e64 s[60:61], s17, v43
	v_cmp_eq_u32_e64 s[68:69], s17, v43
	v_cmpx_lt_i32_e32 vcc, 0x202, v134
	v_cmp_lt_u32_e64 s[62:63], s17, v44
	v_cmp_eq_u32_e64 s[72:73], s17, v44
	v_cmpx_lt_i32_e32 vcc, 0x203, v134
	v_cmp_lt_u32_e64 s[64:65], s17, v45
	v_cmp_eq_u32_e64 s[74:75], s17, v45
	s_mov_b64 exec, -1
	s_or_b64 s[4:5], s[66:67], s[68:69]
	s_or_b64 s[6:7], s[72:73], s[74:75]
	s_or_b64 s[4:5], s[4:5], s[6:7]
	s_cmp_lg_u64 s[4:5], 0
	s_cbranch_scc0 .Lsel_ft_st2
	v_mov_b32_e32 v136, s27
	v_mbcnt_lo_u32_b32 v136, s66, v136
	v_mbcnt_hi_u32_b32 v136, s67, v136
	v_mbcnt_lo_u32_b32 v136, s68, v136
	v_mbcnt_hi_u32_b32 v136, s69, v136
	v_mbcnt_lo_u32_b32 v136, s72, v136
	v_mbcnt_hi_u32_b32 v136, s73, v136
	v_mbcnt_lo_u32_b32 v136, s74, v136
	v_mbcnt_hi_u32_b32 v136, s75, v136
	s_mov_b64 exec, s[66:67]
	v_cmp_gt_u32_e64 s[4:5], s15, v136
	v_add_u32_e32 v136, 1, v136
	s_or_b64 s[58:59], s[58:59], s[4:5]
	s_mov_b64 exec, s[68:69]
	v_cmp_gt_u32_e64 s[4:5], s15, v136
	v_add_u32_e32 v136, 1, v136
	s_or_b64 s[60:61], s[60:61], s[4:5]
	s_mov_b64 exec, s[72:73]
	v_cmp_gt_u32_e64 s[4:5], s15, v136
	v_add_u32_e32 v136, 1, v136
	s_or_b64 s[62:63], s[62:63], s[4:5]
	s_mov_b64 exec, s[74:75]
	v_cmp_gt_u32_e64 s[4:5], s15, v136
	v_add_u32_e32 v136, 1, v136
	s_or_b64 s[64:65], s[64:65], s[4:5]
	s_mov_b64 exec, -1
	s_bcnt1_i32_b64 s4, s[66:67]
	s_add_i32 s27, s27, s4
	s_bcnt1_i32_b64 s4, s[68:69]
	s_add_i32 s27, s27, s4
	s_bcnt1_i32_b64 s4, s[72:73]
	s_add_i32 s27, s27, s4
	s_bcnt1_i32_b64 s4, s[74:75]
	s_add_i32 s27, s27, s4
.Lsel_ft_st2:
	v_mov_b32_e32 v135, s26
	v_mbcnt_lo_u32_b32 v135, s58, v135
	v_mbcnt_hi_u32_b32 v135, s59, v135
	v_mbcnt_lo_u32_b32 v135, s60, v135
	v_mbcnt_hi_u32_b32 v135, s61, v135
	v_mbcnt_lo_u32_b32 v135, s62, v135
	v_mbcnt_hi_u32_b32 v135, s63, v135
	v_mbcnt_lo_u32_b32 v135, s64, v135
	v_mbcnt_hi_u32_b32 v135, s65, v135
	s_mov_b64 exec, s[58:59]
	v_lshlrev_b32_e32 v137, 2, v135
	v_add_u32_e32 v135, 1, v135
	v_add_u32_e32 v141, 0x200, v145
	v_cmpx_gt_u32_e32 vcc, 0x400, v137
	global_store_dword v137, v141, s[40:41]
	s_mov_b64 exec, s[60:61]
	v_lshlrev_b32_e32 v138, 2, v135
	v_add_u32_e32 v135, 1, v135
	v_add_u32_e32 v142, 0x201, v145
	v_cmpx_gt_u32_e32 vcc, 0x400, v138
	global_store_dword v138, v142, s[40:41]
	s_mov_b64 exec, s[62:63]
	v_lshlrev_b32_e32 v139, 2, v135
	v_add_u32_e32 v135, 1, v135
	v_add_u32_e32 v143, 0x202, v145
	v_cmpx_gt_u32_e32 vcc, 0x400, v139
	global_store_dword v139, v143, s[40:41]
	s_mov_b64 exec, s[64:65]
	v_lshlrev_b32_e32 v140, 2, v135
	v_add_u32_e32 v135, 1, v135
	v_add_u32_e32 v144, 0x203, v145
	v_cmpx_gt_u32_e32 vcc, 0x400, v140
	global_store_dword v140, v144, s[40:41]
	s_mov_b64 exec, -1
	s_bcnt1_i32_b64 s4, s[58:59]
	s_add_i32 s26, s26, s4
	s_bcnt1_i32_b64 s4, s[60:61]
	s_add_i32 s26, s26, s4
	s_bcnt1_i32_b64 s4, s[62:63]
	s_add_i32 s26, s26, s4
	s_bcnt1_i32_b64 s4, s[64:65]
	s_add_i32 s26, s26, s4
	v_ashrrev_i32_e32 v46, 31, v30
	v_or_b32_e32 v46, 0x80000000, v46
	v_xor_b32_e32 v46, v30, v46
	v_ashrrev_i32_e32 v47, 31, v31
	v_or_b32_e32 v47, 0x80000000, v47
	v_xor_b32_e32 v47, v31, v47
	v_ashrrev_i32_e32 v48, 31, v32
	v_or_b32_e32 v48, 0x80000000, v48
	v_xor_b32_e32 v48, v32, v48
	v_ashrrev_i32_e32 v49, 31, v33
	v_or_b32_e32 v49, 0x80000000, v49
	v_xor_b32_e32 v49, v33, v49
	v_cmpx_lt_i32_e32 vcc, 0x300, v134
	v_cmp_lt_u32_e64 s[58:59], s17, v46
	v_cmp_eq_u32_e64 s[66:67], s17, v46
	v_cmpx_lt_i32_e32 vcc, 0x301, v134
	v_cmp_lt_u32_e64 s[60:61], s17, v47
	v_cmp_eq_u32_e64 s[68:69], s17, v47
	v_cmpx_lt_i32_e32 vcc, 0x302, v134
	v_cmp_lt_u32_e64 s[62:63], s17, v48
	v_cmp_eq_u32_e64 s[72:73], s17, v48
	v_cmpx_lt_i32_e32 vcc, 0x303, v134
	v_cmp_lt_u32_e64 s[64:65], s17, v49
	v_cmp_eq_u32_e64 s[74:75], s17, v49
	s_mov_b64 exec, -1
	s_or_b64 s[4:5], s[66:67], s[68:69]
	s_or_b64 s[6:7], s[72:73], s[74:75]
	s_or_b64 s[4:5], s[4:5], s[6:7]
	s_cmp_lg_u64 s[4:5], 0
	s_cbranch_scc0 .Lsel_ft_st3
	v_mov_b32_e32 v136, s27
	v_mbcnt_lo_u32_b32 v136, s66, v136
	v_mbcnt_hi_u32_b32 v136, s67, v136
	v_mbcnt_lo_u32_b32 v136, s68, v136
	v_mbcnt_hi_u32_b32 v136, s69, v136
	v_mbcnt_lo_u32_b32 v136, s72, v136
	v_mbcnt_hi_u32_b32 v136, s73, v136
	v_mbcnt_lo_u32_b32 v136, s74, v136
	v_mbcnt_hi_u32_b32 v136, s75, v136
	s_mov_b64 exec, s[66:67]
	v_cmp_gt_u32_e64 s[4:5], s15, v136
	v_add_u32_e32 v136, 1, v136
	s_or_b64 s[58:59], s[58:59], s[4:5]
	s_mov_b64 exec, s[68:69]
	v_cmp_gt_u32_e64 s[4:5], s15, v136
	v_add_u32_e32 v136, 1, v136
	s_or_b64 s[60:61], s[60:61], s[4:5]
	s_mov_b64 exec, s[72:73]
	v_cmp_gt_u32_e64 s[4:5], s15, v136
	v_add_u32_e32 v136, 1, v136
	s_or_b64 s[62:63], s[62:63], s[4:5]
	s_mov_b64 exec, s[74:75]
	v_cmp_gt_u32_e64 s[4:5], s15, v136
	v_add_u32_e32 v136, 1, v136
	s_or_b64 s[64:65], s[64:65], s[4:5]
	s_mov_b64 exec, -1
	s_bcnt1_i32_b64 s4, s[66:67]
	s_add_i32 s27, s27, s4
	s_bcnt1_i32_b64 s4, s[68:69]
	s_add_i32 s27, s27, s4
	s_bcnt1_i32_b64 s4, s[72:73]
	s_add_i32 s27, s27, s4
	s_bcnt1_i32_b64 s4, s[74:75]
	s_add_i32 s27, s27, s4
.Lsel_ft_st3:
	v_mov_b32_e32 v135, s26
	v_mbcnt_lo_u32_b32 v135, s58, v135
	v_mbcnt_hi_u32_b32 v135, s59, v135
	v_mbcnt_lo_u32_b32 v135, s60, v135
	v_mbcnt_hi_u32_b32 v135, s61, v135
	v_mbcnt_lo_u32_b32 v135, s62, v135
	v_mbcnt_hi_u32_b32 v135, s63, v135
	v_mbcnt_lo_u32_b32 v135, s64, v135
	v_mbcnt_hi_u32_b32 v135, s65, v135
	s_mov_b64 exec, s[58:59]
	v_lshlrev_b32_e32 v137, 2, v135
	v_add_u32_e32 v135, 1, v135
	v_add_u32_e32 v141, 0x300, v145
	v_cmpx_gt_u32_e32 vcc, 0x400, v137
	global_store_dword v137, v141, s[40:41]
	s_mov_b64 exec, s[60:61]
	v_lshlrev_b32_e32 v138, 2, v135
	v_add_u32_e32 v135, 1, v135
	v_add_u32_e32 v142, 0x301, v145
	v_cmpx_gt_u32_e32 vcc, 0x400, v138
	global_store_dword v138, v142, s[40:41]
	s_mov_b64 exec, s[62:63]
	v_lshlrev_b32_e32 v139, 2, v135
	v_add_u32_e32 v135, 1, v135
	v_add_u32_e32 v143, 0x302, v145
	v_cmpx_gt_u32_e32 vcc, 0x400, v139
	global_store_dword v139, v143, s[40:41]
	s_mov_b64 exec, s[64:65]
	v_lshlrev_b32_e32 v140, 2, v135
	v_add_u32_e32 v135, 1, v135
	v_add_u32_e32 v144, 0x303, v145
	v_cmpx_gt_u32_e32 vcc, 0x400, v140
	global_store_dword v140, v144, s[40:41]
	s_mov_b64 exec, -1
	s_bcnt1_i32_b64 s4, s[58:59]
	s_add_i32 s26, s26, s4
	s_bcnt1_i32_b64 s4, s[60:61]
	s_add_i32 s26, s26, s4
	s_bcnt1_i32_b64 s4, s[62:63]
	s_add_i32 s26, s26, s4
	s_bcnt1_i32_b64 s4, s[64:65]
	s_add_i32 s26, s26, s4
